# dead-code pass over the four grouped-GEMM epilogues: 19 sign-extension VALU ops that only fed the replaced 64-bit address chains removed
# speedup vs baseline: 1.0041x; 1.0041x over previous
.LBB0_1546:
	s_mov_b32 s73, 0xc2700000
	v_mov_b32_e32 v184, 0x41898193
	v_lshlrev_b32_e32 v150, 16, v86
	v_and_b32_e32 v151, 0xffff0000, v86
	v_mul_f32_e32 v158, 0x3d800000, v177
	v_pk_fma_f32 v[130:131], v[158:159], v[130:131], v[150:151] op_sel_hi:[0,1,1]
	v_med3_f32 v130, v130, s73, v184
	v_med3_f32 v131, v131, s73, v184
	v_exp_f32_e64 v178, -v130
	v_exp_f32_e64 v179, -v131
	v_lshlrev_b32_e32 v156, 16, v87
	v_and_b32_e32 v157, 0xffff0000, v87
	v_lshlrev_b32_e32 v152, 16, v82
	v_pk_add_f32 v[178:179], v[178:179], 1.0 op_sel_hi:[1,0]
	v_and_b32_e32 v153, 0xffff0000, v82
	v_lshlrev_b32_e32 v154, 16, v83
	v_and_b32_e32 v155, 0xffff0000, v83
	v_pk_fma_f32 v[132:133], v[158:159], v[132:133], v[156:157] op_sel_hi:[0,1,1]
	v_pk_fma_f32 v[134:135], v[158:159], v[134:135], v[152:153] op_sel_hi:[0,1,1]
	v_pk_fma_f32 v[136:137], v[158:159], v[136:137], v[154:155] op_sel_hi:[0,1,1]
	v_med3_f32 v134, v134, s70, v167
	v_med3_f32 v135, v135, s70, v167
	v_med3_f32 v132, v132, s73, v184
	v_med3_f32 v133, v133, s73, v184
	v_pk_mul_f32 v[130:131], v[130:131], v[134:135]
	v_med3_f32 v134, v136, s70, v167
	v_med3_f32 v135, v137, s70, v167
	v_exp_f32_e64 v136, -v132
	v_exp_f32_e64 v137, -v133
	v_lshlrev_b32_e32 v86, 16, v88
	v_and_b32_e32 v87, 0xffff0000, v88
	v_pk_fma_f32 v[122:123], v[158:159], v[122:123], v[86:87] op_sel_hi:[0,1,1]
	v_pk_add_f32 v[136:137], v[136:137], 1.0 op_sel_hi:[1,0]
	v_med3_f32 v122, v122, s73, v184
	v_pk_mul_f32 v[180:181], v[178:179], v[136:137]
	v_rcp_f32_e32 v180, v180
	v_rcp_f32_e32 v181, v181
	s_nop 0
	v_pk_mul_f32 v[182:183], v[180:181], v[136:137]
	v_pk_mul_f32 v[136:137], v[180:181], v[178:179]
	v_pk_mul_f32 v[130:131], v[130:131], v[182:183]
	v_med3_f32 v123, v123, s73, v184
	v_lshlrev_b32_e32 v88, 16, v89
	v_and_b32_e32 v89, 0xffff0000, v89
	v_pk_mul_f32 v[132:133], v[132:133], v[136:137]
	v_lshlrev_b32_e32 v82, 16, v84
	v_pk_mul_f32 v[132:133], v[132:133], v[134:135]
	v_exp_f32_e64 v134, -v122
	v_exp_f32_e64 v135, -v123
	v_and_b32_e32 v83, 0xffff0000, v84
	v_lshlrev_b32_e32 v84, 16, v85
	v_and_b32_e32 v85, 0xffff0000, v85
	v_pk_add_f32 v[134:135], v[134:135], 1.0 op_sel_hi:[1,0]
	v_pk_fma_f32 v[124:125], v[158:159], v[124:125], v[88:89] op_sel_hi:[0,1,1]
	v_pk_fma_f32 v[126:127], v[158:159], v[126:127], v[82:83] op_sel_hi:[0,1,1]
	v_pk_fma_f32 v[128:129], v[158:159], v[128:129], v[84:85] op_sel_hi:[0,1,1]
	v_med3_f32 v126, v126, s70, v167
	v_med3_f32 v127, v127, s70, v167
	v_med3_f32 v124, v124, s73, v184
	v_med3_f32 v125, v125, s73, v184
	v_pk_mul_f32 v[122:123], v[122:123], v[126:127]
	v_med3_f32 v126, v128, s70, v167
	v_med3_f32 v127, v129, s70, v167
	v_exp_f32_e64 v128, -v124
	v_exp_f32_e64 v129, -v125
	v_mov_b32_e32 v142, v0
	s_and_b64 vcc, exec, s[6:7]
	v_pk_add_f32 v[128:129], v[128:129], 1.0 op_sel_hi:[1,0]
	v_readfirstlane_b32 s69, v142
	v_pk_mul_f32 v[180:181], v[134:135], v[128:129]
	v_rcp_f32_e32 v180, v180
	v_rcp_f32_e32 v181, v181
	s_nop 0
	v_pk_mul_f32 v[182:183], v[180:181], v[128:129]
	v_pk_mul_f32 v[128:129], v[180:181], v[134:135]
	v_pk_mul_f32 v[122:123], v[122:123], v[182:183]
	s_ashr_i32 s8, s69, 6
	s_mul_i32 s9, s8, 0xb00
	s_add_i32 s71, s9, 0
	v_pk_mul_f32 v[124:125], v[124:125], v[128:129]
	v_and_b32_e32 v147, 15, v142
	v_pk_mul_f32 v[124:125], v[124:125], v[126:127]
	v_cvt_pk_fp8_f32 v126, v130, v131
	v_cvt_pk_fp8_f32 v127, v122, v123
	v_lshrrev_b32_e32 v123, 1, v142
	s_add_i32 s71, s71, 0x20000
	v_cvt_pk_fp8_f32 v126, v132, v133 op_sel:[0,0,1]
	v_cvt_pk_fp8_f32 v127, v124, v125 op_sel:[0,0,1]
	v_mul_f32_e32 v124, 0x3d800000, v176
	v_mul_u32_u24_e32 v122, 48, v147
	v_and_b32_e32 v123, 24, v123
	v_pk_fma_f32 v[114:115], v[124:125], v[114:115], v[150:151] op_sel_hi:[0,1,1]
	v_add3_u32 v122, s71, v122, v123
	v_med3_f32 v114, v114, s73, v184
	v_med3_f32 v115, v115, s73, v184
	ds_write_b64 v122, v[126:127]
	v_exp_f32_e64 v126, -v114
	v_exp_f32_e64 v127, -v115
	v_pk_fma_f32 v[116:117], v[124:125], v[116:117], v[156:157] op_sel_hi:[0,1,1]
	v_pk_fma_f32 v[118:119], v[124:125], v[118:119], v[152:153] op_sel_hi:[0,1,1]
	v_pk_fma_f32 v[120:121], v[124:125], v[120:121], v[154:155] op_sel_hi:[0,1,1]
	v_pk_add_f32 v[126:127], v[126:127], 1.0 op_sel_hi:[1,0]
	v_med3_f32 v118, v118, s70, v167
	v_med3_f32 v119, v119, s70, v167
	v_med3_f32 v116, v116, s73, v184
	v_med3_f32 v117, v117, s73, v184
	v_pk_fma_f32 v[106:107], v[124:125], v[106:107], v[86:87] op_sel_hi:[0,1,1]
	v_pk_mul_f32 v[114:115], v[114:115], v[118:119]
	v_med3_f32 v118, v120, s70, v167
	v_med3_f32 v119, v121, s70, v167
	v_exp_f32_e64 v120, -v116
	v_exp_f32_e64 v121, -v117
	v_med3_f32 v106, v106, s73, v184
	v_med3_f32 v107, v107, s73, v184
	v_pk_fma_f32 v[108:109], v[124:125], v[108:109], v[88:89] op_sel_hi:[0,1,1]
	v_pk_add_f32 v[120:121], v[120:121], 1.0 op_sel_hi:[1,0]
	v_pk_fma_f32 v[110:111], v[124:125], v[110:111], v[82:83] op_sel_hi:[0,1,1]
	v_pk_mul_f32 v[180:181], v[126:127], v[120:121]
	v_rcp_f32_e32 v180, v180
	v_rcp_f32_e32 v181, v181
	s_nop 0
	v_pk_mul_f32 v[182:183], v[180:181], v[120:121]
	v_pk_mul_f32 v[120:121], v[180:181], v[126:127]
	v_pk_mul_f32 v[114:115], v[114:115], v[182:183]
	v_pk_fma_f32 v[112:113], v[124:125], v[112:113], v[84:85] op_sel_hi:[0,1,1]
	v_med3_f32 v110, v110, s70, v167
	v_med3_f32 v111, v111, s70, v167
	v_pk_mul_f32 v[116:117], v[116:117], v[120:121]
	v_med3_f32 v108, v108, s73, v184
	v_pk_mul_f32 v[116:117], v[116:117], v[118:119]
	v_exp_f32_e64 v118, -v106
	v_exp_f32_e64 v119, -v107
	v_med3_f32 v109, v109, s73, v184
	s_ashr_i32 s69, s69, 2
	s_andn2_b32 s69, s69, 63
	v_pk_add_f32 v[118:119], v[118:119], 1.0 op_sel_hi:[1,0]
	s_lshl_b32 s8, s8, 5
	s_lshl_b32 s9, s80, 7
	s_and_b32 s8, s8, 0x60
	s_or_b32 s8, s8, s9
	s_ashr_i32 s9, s8, 31
	v_pk_mul_f32 v[106:107], v[106:107], v[110:111]
	v_med3_f32 v110, v112, s70, v167
	v_med3_f32 v111, v113, s70, v167
	v_exp_f32_e64 v112, -v108
	v_exp_f32_e64 v113, -v109
	s_nop 0
	v_pk_add_f32 v[112:113], v[112:113], 1.0 op_sel_hi:[1,0]
	s_nop 0
	v_pk_mul_f32 v[180:181], v[118:119], v[112:113]
	v_rcp_f32_e32 v180, v180
	v_rcp_f32_e32 v181, v181
	s_nop 0
	v_pk_mul_f32 v[182:183], v[180:181], v[112:113]
	v_pk_mul_f32 v[112:113], v[180:181], v[118:119]
	v_pk_mul_f32 v[106:107], v[106:107], v[182:183]
	s_nop 0
	v_pk_mul_f32 v[108:109], v[108:109], v[112:113]
	s_nop 0
	v_pk_mul_f32 v[108:109], v[108:109], v[110:111]
	v_cvt_pk_fp8_f32 v110, v114, v115
	v_cvt_pk_fp8_f32 v111, v106, v107
	v_bfe_u32 v106, v142, 1, 5
	v_mul_u32_u24_e32 v107, 48, v106
	v_cvt_pk_fp8_f32 v110, v116, v117 op_sel:[0,0,1]
	v_cvt_pk_fp8_f32 v111, v108, v109 op_sel:[0,0,1]
	v_lshlrev_b32_e32 v108, 4, v142
	v_and_b32_e32 v142, 16, v108
	v_lshl_or_b32 v106, s78, 8, v106
	ds_write_b64 v122, v[110:111] offset:768
	v_add3_u32 v108, s71, v107, v142
	v_add_u32_e32 v106, s69, v106
	ds_read_b128 v[110:113], v108
	v_ashrrev_i32_e32 v107, 31, v106
	v_lshl_add_u32 v114, v106, 10, v142
	s_add_u32 s86, s16, s8
	s_addc_u32 s87, s17, s9
	s_waitcnt lgkmcnt(0)
	global_store_dwordx4 v114, v[110:113], s[86:87]
	s_nop 1
	v_mul_f32_e32 v110, 0x3d800000, v175
	v_pk_fma_f32 v[98:99], v[110:111], v[98:99], v[150:151] op_sel_hi:[0,1,1]
	v_med3_f32 v98, v98, s73, v184
	v_med3_f32 v99, v99, s73, v184
	v_exp_f32_e64 v112, -v98
	v_exp_f32_e64 v113, -v99
	v_pk_fma_f32 v[100:101], v[110:111], v[100:101], v[156:157] op_sel_hi:[0,1,1]
	v_pk_fma_f32 v[102:103], v[110:111], v[102:103], v[152:153] op_sel_hi:[0,1,1]
	v_pk_fma_f32 v[104:105], v[110:111], v[104:105], v[154:155] op_sel_hi:[0,1,1]
	v_pk_add_f32 v[112:113], v[112:113], 1.0 op_sel_hi:[1,0]
	v_med3_f32 v102, v102, s70, v167
	v_med3_f32 v103, v103, s70, v167
	v_med3_f32 v100, v100, s73, v184
	v_med3_f32 v101, v101, s73, v184
	v_pk_fma_f32 v[90:91], v[110:111], v[90:91], v[86:87] op_sel_hi:[0,1,1]
	v_pk_mul_f32 v[98:99], v[98:99], v[102:103]
	v_med3_f32 v102, v104, s70, v167
	v_med3_f32 v103, v105, s70, v167
	v_exp_f32_e64 v104, -v100
	v_exp_f32_e64 v105, -v101
	v_med3_f32 v90, v90, s73, v184
	v_med3_f32 v91, v91, s73, v184
	v_pk_fma_f32 v[92:93], v[110:111], v[92:93], v[88:89] op_sel_hi:[0,1,1]
	v_pk_add_f32 v[104:105], v[104:105], 1.0 op_sel_hi:[1,0]
	v_pk_fma_f32 v[94:95], v[110:111], v[94:95], v[82:83] op_sel_hi:[0,1,1]
	v_pk_mul_f32 v[180:181], v[112:113], v[104:105]
	v_rcp_f32_e32 v180, v180
	v_rcp_f32_e32 v181, v181
	s_nop 0
	v_pk_mul_f32 v[182:183], v[180:181], v[104:105]
	v_pk_mul_f32 v[104:105], v[180:181], v[112:113]
	v_pk_mul_f32 v[98:99], v[98:99], v[182:183]
	v_pk_fma_f32 v[96:97], v[110:111], v[96:97], v[84:85] op_sel_hi:[0,1,1]
	v_med3_f32 v94, v94, s70, v167
	v_med3_f32 v95, v95, s70, v167
	v_pk_mul_f32 v[100:101], v[100:101], v[104:105]
	v_med3_f32 v92, v92, s73, v184
	v_pk_mul_f32 v[100:101], v[100:101], v[102:103]
	v_exp_f32_e64 v102, -v90
	v_exp_f32_e64 v103, -v91
	v_med3_f32 v93, v93, s73, v184
	v_pk_add_f32 v[102:103], v[102:103], 1.0 op_sel_hi:[1,0]
	s_nop 0
	s_nop 0
	s_nop 0
	v_pk_mul_f32 v[90:91], v[90:91], v[94:95]
	v_med3_f32 v94, v96, s70, v167
	v_med3_f32 v95, v97, s70, v167
	v_exp_f32_e64 v96, -v92
	v_exp_f32_e64 v97, -v93
	s_nop 0
	v_pk_add_f32 v[96:97], v[96:97], 1.0 op_sel_hi:[1,0]
	s_nop 0
	v_pk_mul_f32 v[180:181], v[102:103], v[96:97]
	v_rcp_f32_e32 v180, v180
	v_rcp_f32_e32 v181, v181
	s_nop 0
	v_pk_mul_f32 v[182:183], v[180:181], v[96:97]
	v_pk_mul_f32 v[96:97], v[180:181], v[102:103]
	v_pk_mul_f32 v[90:91], v[90:91], v[182:183]
	s_nop 0
	v_pk_mul_f32 v[92:93], v[92:93], v[96:97]
	s_nop 0
	v_pk_mul_f32 v[92:93], v[92:93], v[94:95]
	v_cvt_pk_fp8_f32 v95, v90, v91
	v_mul_f32_e32 v90, 0x3d800000, v174
	v_pk_fma_f32 v[74:75], v[90:91], v[74:75], v[150:151] op_sel_hi:[0,1,1]
	v_med3_f32 v74, v74, s73, v184
	v_med3_f32 v75, v75, s73, v184
	v_cvt_pk_fp8_f32 v95, v92, v93 op_sel:[0,0,1]
	v_exp_f32_e64 v92, -v74
	v_exp_f32_e64 v93, -v75
	v_pk_fma_f32 v[76:77], v[90:91], v[76:77], v[156:157] op_sel_hi:[0,1,1]
	v_pk_fma_f32 v[78:79], v[90:91], v[78:79], v[152:153] op_sel_hi:[0,1,1]
	v_pk_fma_f32 v[80:81], v[90:91], v[80:81], v[154:155] op_sel_hi:[0,1,1]
	v_pk_add_f32 v[92:93], v[92:93], 1.0 op_sel_hi:[1,0]
	v_med3_f32 v78, v78, s70, v167
	v_med3_f32 v79, v79, s70, v167
	v_med3_f32 v76, v76, s73, v184
	v_med3_f32 v77, v77, s73, v184
	v_pk_fma_f32 v[66:67], v[90:91], v[66:67], v[86:87] op_sel_hi:[0,1,1]
	v_pk_mul_f32 v[74:75], v[74:75], v[78:79]
	v_med3_f32 v78, v80, s70, v167
	v_med3_f32 v79, v81, s70, v167
	v_exp_f32_e64 v80, -v76
	v_exp_f32_e64 v81, -v77
	v_med3_f32 v66, v66, s73, v184
	v_med3_f32 v67, v67, s73, v184
	v_pk_fma_f32 v[68:69], v[90:91], v[68:69], v[88:89] op_sel_hi:[0,1,1]
	v_pk_add_f32 v[80:81], v[80:81], 1.0 op_sel_hi:[1,0]
	v_pk_fma_f32 v[70:71], v[90:91], v[70:71], v[82:83] op_sel_hi:[0,1,1]
	v_pk_mul_f32 v[180:181], v[92:93], v[80:81]
	v_rcp_f32_e32 v180, v180
	v_rcp_f32_e32 v181, v181
	s_nop 0
	v_pk_mul_f32 v[182:183], v[180:181], v[80:81]
	v_pk_mul_f32 v[80:81], v[180:181], v[92:93]
	v_pk_mul_f32 v[74:75], v[74:75], v[182:183]
	v_pk_fma_f32 v[72:73], v[90:91], v[72:73], v[84:85] op_sel_hi:[0,1,1]
	v_med3_f32 v70, v70, s70, v167
	v_med3_f32 v71, v71, s70, v167
	v_pk_mul_f32 v[76:77], v[76:77], v[80:81]
	v_med3_f32 v68, v68, s73, v184
	v_pk_mul_f32 v[76:77], v[76:77], v[78:79]
	v_exp_f32_e64 v78, -v66
	v_exp_f32_e64 v79, -v67
	v_med3_f32 v69, v69, s73, v184
	v_cvt_pk_fp8_f32 v94, v98, v99
	v_pk_add_f32 v[78:79], v[78:79], 1.0 op_sel_hi:[1,0]
	v_cvt_pk_fp8_f32 v94, v100, v101 op_sel:[0,0,1]
	ds_write_b64 v122, v[94:95]
	s_nop 0
	v_pk_mul_f32 v[66:67], v[66:67], v[70:71]
	v_med3_f32 v70, v72, s70, v167
	v_med3_f32 v71, v73, s70, v167
	v_exp_f32_e64 v72, -v68
	v_exp_f32_e64 v73, -v69
	s_nop 0
	v_pk_add_f32 v[72:73], v[72:73], 1.0 op_sel_hi:[1,0]
	s_nop 0
	v_pk_mul_f32 v[180:181], v[78:79], v[72:73]
	v_rcp_f32_e32 v180, v180
	v_rcp_f32_e32 v181, v181
	s_nop 0
	v_pk_mul_f32 v[182:183], v[180:181], v[72:73]
	v_pk_mul_f32 v[72:73], v[180:181], v[78:79]
	v_pk_mul_f32 v[66:67], v[66:67], v[182:183]
	s_nop 0
	v_pk_mul_f32 v[68:69], v[68:69], v[72:73]
	s_nop 0
	v_pk_mul_f32 v[68:69], v[68:69], v[70:71]
	v_cvt_pk_fp8_f32 v70, v74, v75
	v_cvt_pk_fp8_f32 v71, v66, v67
	v_cvt_pk_fp8_f32 v70, v76, v77 op_sel:[0,0,1]
	v_cvt_pk_fp8_f32 v71, v68, v69 op_sel:[0,0,1]
	ds_write_b64 v122, v[70:71] offset:768
	v_or_b32_e32 v70, 32, v106
	ds_read_b128 v[66:69], v108
	v_ashrrev_i32_e32 v71, 31, v70
	v_lshl_add_u32 v70, v70, 10, v142
	s_add_u32 s86, s16, s8
	s_addc_u32 s87, s17, s9
	s_waitcnt lgkmcnt(0)
	global_store_dwordx4 v70, v[66:69], s[86:87]
	s_nop 1
	v_mul_f32_e32 v66, 0x3d800000, v173
	v_pk_fma_f32 v[58:59], v[66:67], v[58:59], v[150:151] op_sel_hi:[0,1,1]
	v_med3_f32 v58, v58, s73, v184
	v_med3_f32 v59, v59, s73, v184
	v_exp_f32_e64 v68, -v58
	v_exp_f32_e64 v69, -v59
	v_pk_fma_f32 v[60:61], v[66:67], v[60:61], v[156:157] op_sel_hi:[0,1,1]
	v_pk_fma_f32 v[62:63], v[66:67], v[62:63], v[152:153] op_sel_hi:[0,1,1]
	v_pk_fma_f32 v[64:65], v[66:67], v[64:65], v[154:155] op_sel_hi:[0,1,1]
	v_pk_add_f32 v[68:69], v[68:69], 1.0 op_sel_hi:[1,0]
	v_med3_f32 v62, v62, s70, v167
	v_med3_f32 v63, v63, s70, v167
	v_med3_f32 v60, v60, s73, v184
	v_med3_f32 v61, v61, s73, v184
	v_pk_fma_f32 v[50:51], v[66:67], v[50:51], v[86:87] op_sel_hi:[0,1,1]
	v_pk_mul_f32 v[58:59], v[58:59], v[62:63]
	v_med3_f32 v62, v64, s70, v167
	v_med3_f32 v63, v65, s70, v167
	v_exp_f32_e64 v64, -v60
	v_exp_f32_e64 v65, -v61
	v_med3_f32 v50, v50, s73, v184
	v_med3_f32 v51, v51, s73, v184
	v_pk_fma_f32 v[52:53], v[66:67], v[52:53], v[88:89] op_sel_hi:[0,1,1]
	v_pk_add_f32 v[64:65], v[64:65], 1.0 op_sel_hi:[1,0]
	v_pk_fma_f32 v[54:55], v[66:67], v[54:55], v[82:83] op_sel_hi:[0,1,1]
	v_pk_mul_f32 v[180:181], v[68:69], v[64:65]
	v_rcp_f32_e32 v180, v180
	v_rcp_f32_e32 v181, v181
	s_nop 0
	v_pk_mul_f32 v[182:183], v[180:181], v[64:65]
	v_pk_mul_f32 v[64:65], v[180:181], v[68:69]
	v_pk_mul_f32 v[58:59], v[58:59], v[182:183]
	v_pk_fma_f32 v[56:57], v[66:67], v[56:57], v[84:85] op_sel_hi:[0,1,1]
	v_med3_f32 v54, v54, s70, v167
	v_med3_f32 v55, v55, s70, v167
	v_pk_mul_f32 v[60:61], v[60:61], v[64:65]
	v_med3_f32 v52, v52, s73, v184
	v_pk_mul_f32 v[60:61], v[60:61], v[62:63]
	v_exp_f32_e64 v62, -v50
	v_exp_f32_e64 v63, -v51
	v_med3_f32 v53, v53, s73, v184
	v_pk_add_f32 v[62:63], v[62:63], 1.0 op_sel_hi:[1,0]
	s_nop 0
	s_nop 0
	s_nop 0
	v_pk_mul_f32 v[50:51], v[50:51], v[54:55]
	v_med3_f32 v54, v56, s70, v167
	v_med3_f32 v55, v57, s70, v167
	v_exp_f32_e64 v56, -v52
	v_exp_f32_e64 v57, -v53
	s_nop 0
	v_pk_add_f32 v[56:57], v[56:57], 1.0 op_sel_hi:[1,0]
	s_nop 0
	v_pk_mul_f32 v[180:181], v[62:63], v[56:57]
	v_rcp_f32_e32 v180, v180
	v_rcp_f32_e32 v181, v181
	s_nop 0
	v_pk_mul_f32 v[182:183], v[180:181], v[56:57]
	v_pk_mul_f32 v[56:57], v[180:181], v[62:63]
	v_pk_mul_f32 v[50:51], v[50:51], v[182:183]
	s_nop 0
	v_pk_mul_f32 v[52:53], v[52:53], v[56:57]
	s_nop 0
	v_pk_mul_f32 v[52:53], v[52:53], v[54:55]
	v_cvt_pk_fp8_f32 v55, v50, v51
	v_mul_f32_e32 v50, 0x3d800000, v172
	v_pk_fma_f32 v[42:43], v[50:51], v[42:43], v[150:151] op_sel_hi:[0,1,1]
	v_med3_f32 v42, v42, s73, v184
	v_med3_f32 v43, v43, s73, v184
	v_cvt_pk_fp8_f32 v55, v52, v53 op_sel:[0,0,1]
	v_exp_f32_e64 v52, -v42
	v_exp_f32_e64 v53, -v43
	v_pk_fma_f32 v[44:45], v[50:51], v[44:45], v[156:157] op_sel_hi:[0,1,1]
	v_pk_fma_f32 v[46:47], v[50:51], v[46:47], v[152:153] op_sel_hi:[0,1,1]
	v_pk_fma_f32 v[48:49], v[50:51], v[48:49], v[154:155] op_sel_hi:[0,1,1]
	v_pk_add_f32 v[52:53], v[52:53], 1.0 op_sel_hi:[1,0]
	v_med3_f32 v46, v46, s70, v167
	v_med3_f32 v47, v47, s70, v167
	v_med3_f32 v44, v44, s73, v184
	v_med3_f32 v45, v45, s73, v184
	v_pk_fma_f32 v[34:35], v[50:51], v[34:35], v[86:87] op_sel_hi:[0,1,1]
	v_pk_mul_f32 v[42:43], v[42:43], v[46:47]
	v_med3_f32 v46, v48, s70, v167
	v_med3_f32 v47, v49, s70, v167
	v_exp_f32_e64 v48, -v44
	v_exp_f32_e64 v49, -v45
	v_med3_f32 v34, v34, s73, v184
	v_med3_f32 v35, v35, s73, v184
	v_pk_fma_f32 v[36:37], v[50:51], v[36:37], v[88:89] op_sel_hi:[0,1,1]
	v_pk_add_f32 v[48:49], v[48:49], 1.0 op_sel_hi:[1,0]
	v_pk_fma_f32 v[38:39], v[50:51], v[38:39], v[82:83] op_sel_hi:[0,1,1]
	v_pk_mul_f32 v[180:181], v[52:53], v[48:49]
	v_rcp_f32_e32 v180, v180
	v_rcp_f32_e32 v181, v181
	s_nop 0
	v_pk_mul_f32 v[182:183], v[180:181], v[48:49]
	v_pk_mul_f32 v[48:49], v[180:181], v[52:53]
	v_pk_mul_f32 v[42:43], v[42:43], v[182:183]
	v_pk_fma_f32 v[40:41], v[50:51], v[40:41], v[84:85] op_sel_hi:[0,1,1]
	v_med3_f32 v38, v38, s70, v167
	v_med3_f32 v39, v39, s70, v167
	v_pk_mul_f32 v[44:45], v[44:45], v[48:49]
	v_med3_f32 v36, v36, s73, v184
	v_pk_mul_f32 v[44:45], v[44:45], v[46:47]
	v_exp_f32_e64 v46, -v34
	v_exp_f32_e64 v47, -v35
	v_med3_f32 v37, v37, s73, v184
	v_cvt_pk_fp8_f32 v54, v58, v59
	v_pk_add_f32 v[46:47], v[46:47], 1.0 op_sel_hi:[1,0]
	v_cvt_pk_fp8_f32 v54, v60, v61 op_sel:[0,0,1]
	ds_write_b64 v122, v[54:55]
	s_nop 0
	v_pk_mul_f32 v[34:35], v[34:35], v[38:39]
	v_med3_f32 v38, v40, s70, v167
	v_med3_f32 v39, v41, s70, v167
	v_exp_f32_e64 v40, -v36
	v_exp_f32_e64 v41, -v37
	s_nop 0
	v_pk_add_f32 v[40:41], v[40:41], 1.0 op_sel_hi:[1,0]
	s_nop 0
	v_pk_mul_f32 v[180:181], v[46:47], v[40:41]
	v_rcp_f32_e32 v180, v180
	v_rcp_f32_e32 v181, v181
	s_nop 0
	v_pk_mul_f32 v[182:183], v[180:181], v[40:41]
	v_pk_mul_f32 v[40:41], v[180:181], v[46:47]
	v_pk_mul_f32 v[34:35], v[34:35], v[182:183]
	s_nop 0
	v_pk_mul_f32 v[36:37], v[36:37], v[40:41]
	s_nop 0
	v_pk_mul_f32 v[36:37], v[36:37], v[38:39]
	v_cvt_pk_fp8_f32 v38, v42, v43
	v_cvt_pk_fp8_f32 v39, v34, v35
	v_cvt_pk_fp8_f32 v38, v44, v45 op_sel:[0,0,1]
	v_cvt_pk_fp8_f32 v39, v36, v37 op_sel:[0,0,1]
	ds_write_b64 v122, v[38:39] offset:768
	v_add_u32_e32 v38, 0x80, v106
	ds_read_b128 v[34:37], v108
	v_lshl_add_u32 v38, v38, 10, v142
	s_add_u32 s86, s16, s8
	s_addc_u32 s87, s17, s9
	s_waitcnt lgkmcnt(0)
	global_store_dwordx4 v38, v[34:37], s[86:87]
	s_nop 1
	v_mul_f32_e32 v34, 0x3d800000, v171
	v_pk_fma_f32 v[26:27], v[34:35], v[26:27], v[150:151] op_sel_hi:[0,1,1]
	v_med3_f32 v26, v26, s73, v184
	v_med3_f32 v27, v27, s73, v184
	v_exp_f32_e64 v36, -v26
	v_exp_f32_e64 v37, -v27
	v_pk_fma_f32 v[28:29], v[34:35], v[28:29], v[156:157] op_sel_hi:[0,1,1]
	v_pk_fma_f32 v[30:31], v[34:35], v[30:31], v[152:153] op_sel_hi:[0,1,1]
	v_pk_fma_f32 v[32:33], v[34:35], v[32:33], v[154:155] op_sel_hi:[0,1,1]
	v_pk_add_f32 v[36:37], v[36:37], 1.0 op_sel_hi:[1,0]
	v_med3_f32 v30, v30, s70, v167
	v_med3_f32 v31, v31, s70, v167
	v_med3_f32 v28, v28, s73, v184
	v_med3_f32 v29, v29, s73, v184
	v_pk_fma_f32 v[18:19], v[34:35], v[18:19], v[86:87] op_sel_hi:[0,1,1]
	v_pk_mul_f32 v[26:27], v[26:27], v[30:31]
	v_med3_f32 v30, v32, s70, v167
	v_med3_f32 v31, v33, s70, v167
	v_exp_f32_e64 v32, -v28
	v_exp_f32_e64 v33, -v29
	v_med3_f32 v18, v18, s73, v184
	v_med3_f32 v19, v19, s73, v184
	v_pk_fma_f32 v[20:21], v[34:35], v[20:21], v[88:89] op_sel_hi:[0,1,1]
	v_pk_add_f32 v[32:33], v[32:33], 1.0 op_sel_hi:[1,0]
	v_pk_fma_f32 v[22:23], v[34:35], v[22:23], v[82:83] op_sel_hi:[0,1,1]
	v_pk_mul_f32 v[180:181], v[36:37], v[32:33]
	v_rcp_f32_e32 v180, v180
	v_rcp_f32_e32 v181, v181
	s_nop 0
	v_pk_mul_f32 v[182:183], v[180:181], v[32:33]
	v_pk_mul_f32 v[32:33], v[180:181], v[36:37]
	v_pk_mul_f32 v[26:27], v[26:27], v[182:183]
	v_pk_fma_f32 v[24:25], v[34:35], v[24:25], v[84:85] op_sel_hi:[0,1,1]
	v_med3_f32 v22, v22, s70, v167
	v_med3_f32 v23, v23, s70, v167
	v_pk_mul_f32 v[28:29], v[28:29], v[32:33]
	v_med3_f32 v20, v20, s73, v184
	v_pk_mul_f32 v[28:29], v[28:29], v[30:31]
	v_exp_f32_e64 v30, -v18
	v_exp_f32_e64 v31, -v19
	v_med3_f32 v21, v21, s73, v184
	v_pk_add_f32 v[30:31], v[30:31], 1.0 op_sel_hi:[1,0]
	s_nop 0
	s_nop 0
	s_nop 0
	v_pk_mul_f32 v[18:19], v[18:19], v[22:23]
	v_med3_f32 v22, v24, s70, v167
	v_med3_f32 v23, v25, s70, v167
	v_exp_f32_e64 v24, -v20
	v_exp_f32_e64 v25, -v21
	s_nop 0
	v_pk_add_f32 v[24:25], v[24:25], 1.0 op_sel_hi:[1,0]
	s_nop 0
	v_pk_mul_f32 v[180:181], v[30:31], v[24:25]
	v_rcp_f32_e32 v180, v180
	v_rcp_f32_e32 v181, v181
	s_nop 0
	v_pk_mul_f32 v[182:183], v[180:181], v[24:25]
	v_pk_mul_f32 v[24:25], v[180:181], v[30:31]
	v_pk_mul_f32 v[18:19], v[18:19], v[182:183]
	s_nop 0
	v_pk_mul_f32 v[20:21], v[20:21], v[24:25]
	s_nop 0
	v_pk_mul_f32 v[20:21], v[20:21], v[22:23]
	v_cvt_pk_fp8_f32 v23, v18, v19
	v_mul_f32_e32 v18, 0x3d800000, v168
	v_pk_fma_f32 v[10:11], v[18:19], v[10:11], v[150:151] op_sel_hi:[0,1,1]
	v_med3_f32 v10, v10, s73, v184
	v_med3_f32 v11, v11, s73, v184
	v_cvt_pk_fp8_f32 v23, v20, v21 op_sel:[0,0,1]
	v_exp_f32_e64 v20, -v10
	v_exp_f32_e64 v21, -v11
	v_pk_fma_f32 v[12:13], v[18:19], v[12:13], v[156:157] op_sel_hi:[0,1,1]
	v_pk_fma_f32 v[14:15], v[18:19], v[14:15], v[152:153] op_sel_hi:[0,1,1]
	v_pk_fma_f32 v[16:17], v[18:19], v[16:17], v[154:155] op_sel_hi:[0,1,1]
	v_pk_add_f32 v[20:21], v[20:21], 1.0 op_sel_hi:[1,0]
	v_med3_f32 v14, v14, s70, v167
	v_med3_f32 v15, v15, s70, v167
	v_med3_f32 v12, v12, s73, v184
	v_med3_f32 v13, v13, s73, v184
	v_pk_fma_f32 v[2:3], v[18:19], v[2:3], v[86:87] op_sel_hi:[0,1,1]
	v_pk_mul_f32 v[10:11], v[10:11], v[14:15]
	v_med3_f32 v14, v16, s70, v167
	v_med3_f32 v15, v17, s70, v167
	v_exp_f32_e64 v16, -v12
	v_exp_f32_e64 v17, -v13
	v_med3_f32 v2, v2, s73, v184
	v_med3_f32 v3, v3, s73, v184
	v_pk_fma_f32 v[4:5], v[18:19], v[4:5], v[88:89] op_sel_hi:[0,1,1]
	v_pk_add_f32 v[16:17], v[16:17], 1.0 op_sel_hi:[1,0]
	v_pk_fma_f32 v[6:7], v[18:19], v[6:7], v[82:83] op_sel_hi:[0,1,1]
	v_pk_mul_f32 v[180:181], v[20:21], v[16:17]
	v_rcp_f32_e32 v180, v180
	v_rcp_f32_e32 v181, v181
	s_nop 0
	v_pk_mul_f32 v[182:183], v[180:181], v[16:17]
	v_pk_mul_f32 v[16:17], v[180:181], v[20:21]
	v_pk_mul_f32 v[10:11], v[10:11], v[182:183]
	v_pk_fma_f32 v[8:9], v[18:19], v[8:9], v[84:85] op_sel_hi:[0,1,1]
	v_med3_f32 v6, v6, s70, v167
	v_med3_f32 v7, v7, s70, v167
	v_pk_mul_f32 v[12:13], v[12:13], v[16:17]
	v_med3_f32 v4, v4, s73, v184
	v_pk_mul_f32 v[12:13], v[12:13], v[14:15]
	v_exp_f32_e64 v14, -v2
	v_exp_f32_e64 v15, -v3
	v_med3_f32 v5, v5, s73, v184
	v_cvt_pk_fp8_f32 v22, v26, v27
	v_pk_add_f32 v[14:15], v[14:15], 1.0 op_sel_hi:[1,0]
	v_cvt_pk_fp8_f32 v22, v28, v29 op_sel:[0,0,1]
	ds_write_b64 v122, v[22:23]
	s_nop 0
	v_pk_mul_f32 v[2:3], v[2:3], v[6:7]
	v_med3_f32 v6, v8, s70, v167
	v_med3_f32 v7, v9, s70, v167
	v_exp_f32_e64 v8, -v4
	v_exp_f32_e64 v9, -v5
	s_nop 0
	v_pk_add_f32 v[8:9], v[8:9], 1.0 op_sel_hi:[1,0]
	s_nop 0
	v_pk_mul_f32 v[180:181], v[14:15], v[8:9]
	v_rcp_f32_e32 v180, v180
	v_rcp_f32_e32 v181, v181
	s_nop 0
	v_pk_mul_f32 v[182:183], v[180:181], v[8:9]
	v_pk_mul_f32 v[8:9], v[180:181], v[14:15]
	v_pk_mul_f32 v[2:3], v[2:3], v[182:183]
	s_nop 0
	v_pk_mul_f32 v[4:5], v[4:5], v[8:9]
	s_nop 0
	v_pk_mul_f32 v[4:5], v[4:5], v[6:7]
	v_cvt_pk_fp8_f32 v6, v10, v11
	v_cvt_pk_fp8_f32 v7, v2, v3
	v_cvt_pk_fp8_f32 v6, v12, v13 op_sel:[0,0,1]
	v_cvt_pk_fp8_f32 v7, v4, v5 op_sel:[0,0,1]
	ds_write_b64 v122, v[6:7] offset:768
	v_add_u32_e32 v6, 0xa0, v106
	ds_read_b128 v[2:5], v108
	v_lshl_add_u32 v6, v6, 10, v142
	s_add_u32 s86, s16, s8
	s_addc_u32 s87, s17, s9
	s_mov_b64 s[8:9], -1
	s_waitcnt lgkmcnt(0)
	global_store_dwordx4 v6, v[2:5], s[86:87]
	s_cbranch_vccnz .LBB0_1537
	s_lshl_b64 s[6:7], s[74:75], 12
	s_add_u32 s9, s33, s6
	s_addc_u32 s69, s54, s7
	s_lshl_b32 s6, s68, 7
	s_ashr_i32 s7, s6, 31
	v_mov_b32_e32 v2, v0
	s_lshl_b64 s[6:7], s[6:7], 1
	s_add_u32 s6, s9, s6
	v_readfirstlane_b32 s8, v2
	s_addc_u32 s7, s69, s7
	s_and_b32 s9, s8, 0xc0
	s_add_u32 s6, s6, s9
	s_addc_u32 s7, s7, 0
	v_and_b32_e32 v3, 48, v2
	global_load_dwordx4 v[86:89], v3, s[6:7]
	global_load_dwordx4 v[82:85], v3, s[6:7] offset:2048
	s_ashr_i32 s7, s8, 2
	s_lshl_b32 s6, s72, 8
	s_andn2_b32 s7, s7, 63
	s_add_i32 s7, s7, s6
	v_and_or_b32 v2, v2, 15, s7
	v_lshlrev_b32_e32 v4, 2, v2
	global_load_dword v177, v4, s[12:13] offset:0
	global_load_dword v176, v4, s[12:13] offset:64
	global_load_dword v175, v4, s[12:13] offset:128
	global_load_dword v174, v4, s[12:13] offset:192
	global_load_dword v173, v4, s[12:13] offset:512
	global_load_dword v172, v4, s[12:13] offset:576
	global_load_dword v171, v4, s[12:13] offset:640
	global_load_dword v168, v4, s[12:13] offset:704
	s_andn2_b64 vcc, exec, s[14:15]
	s_cbranch_vccnz .LBB0_1536
	s_barrier
	s_branch .LBB0_1536

.LBB0_1627:
	v_lshlrev_b32_e32 v158, 16, v6
	v_and_b32_e32 v159, 0xffff0000, v6
	v_lshlrev_b32_e32 v154, 16, v8
	v_and_b32_e32 v155, 0xffff0000, v8
	v_lshlrev_b32_e32 v156, 16, v7
	v_and_b32_e32 v157, 0xffff0000, v7
	v_lshlrev_b32_e32 v152, 16, v9
	v_and_b32_e32 v153, 0xffff0000, v9
	s_waitcnt vmcnt(10)
	v_lshlrev_b32_e32 v6, 16, v4
	v_and_b32_e32 v7, 0xffff0000, v4
	v_mul_f32_e32 v4, 0x41000000, v146
	v_pk_fma_f32 v[134:135], v[134:135], s[36:37], v[158:159] op_sel_hi:[1,0,1]
	v_pk_fma_f32 v[130:131], v[130:131], s[36:37], v[154:155] op_sel_hi:[1,0,1]
	v_pk_fma_f32 v[136:137], v[136:137], s[36:37], v[156:157] op_sel_hi:[1,0,1]
	v_pk_mul_f32 v[134:135], v[4:5], v[134:135] op_sel_hi:[0,1]
	v_pk_fma_f32 v[132:133], v[132:133], s[36:37], v[152:153] op_sel_hi:[1,0,1]
	v_pk_mul_f32 v[130:131], v[4:5], v[130:131] op_sel_hi:[0,1]
	v_lshlrev_b32_e32 v150, 16, v2
	v_and_b32_e32 v151, 0xffff0000, v2
	v_lshlrev_b32_e32 v8, 16, v3
	v_and_b32_e32 v9, 0xffff0000, v3
	v_lshlrev_b32_e32 v2, 16, v5
	v_and_b32_e32 v3, 0xffff0000, v5
	v_pk_mul_f32 v[136:137], v[4:5], v[136:137] op_sel_hi:[0,1]
	v_pk_mul_f32 v[132:133], v[4:5], v[132:133] op_sel_hi:[0,1]
	v_med3_f32 v5, v134, s70, v164
	v_med3_f32 v134, v130, s70, v164
	v_med3_f32 v135, v135, s70, v164
	v_cvt_pk_fp8_f32 v130, v5, v135
	v_med3_f32 v136, v136, s70, v164
	v_med3_f32 v5, v137, s70, v164
	v_pk_fma_f32 v[126:127], v[126:127], s[36:37], v[150:151] op_sel_hi:[1,0,1]
	v_pk_fma_f32 v[128:129], v[128:129], s[36:37], v[8:9] op_sel_hi:[1,0,1]
	v_pk_fma_f32 v[122:123], v[122:123], s[36:37], v[6:7] op_sel_hi:[1,0,1]
	v_pk_fma_f32 v[124:125], v[124:125], s[36:37], v[2:3] op_sel_hi:[1,0,1]
	v_cvt_pk_fp8_f32 v130, v136, v5 op_sel:[0,0,1]
	v_pk_mul_f32 v[128:129], v[4:5], v[128:129] op_sel_hi:[0,1]
	v_pk_mul_f32 v[126:127], v[4:5], v[126:127] op_sel_hi:[0,1]
	v_pk_mul_f32 v[124:125], v[4:5], v[124:125] op_sel_hi:[0,1]
	v_pk_mul_f32 v[4:5], v[4:5], v[122:123] op_sel_hi:[0,1]
	v_med3_f32 v146, v131, s70, v164
	v_med3_f32 v122, v126, s70, v164
	v_med3_f32 v123, v4, s70, v164
	v_med3_f32 v126, v127, s70, v164
	v_med3_f32 v127, v5, s70, v164
	v_cvt_pk_fp8_f32 v131, v134, v146
	v_cvt_pk_fp8_f32 v4, v122, v126
	v_cvt_pk_fp8_f32 v5, v123, v127
	v_mov_b32_e32 v171, v0
	v_med3_f32 v132, v132, s70, v164
	v_readfirstlane_b32 s39, v171
	s_lshr_b32 s6, s39, 6
	v_med3_f32 v133, v133, s70, v164
	v_med3_f32 v128, v128, s70, v164
	v_med3_f32 v124, v124, s70, v164
	v_med3_f32 v122, v129, s70, v164
	v_med3_f32 v123, v125, s70, v164
	s_mulk_i32 s6, 0xb00
	v_cvt_pk_fp8_f32 v131, v132, v133 op_sel:[0,0,1]
	v_cvt_pk_fp8_f32 v4, v128, v122 op_sel:[0,0,1]
	v_cvt_pk_fp8_f32 v5, v124, v123 op_sel:[0,0,1]
	s_add_i32 s6, s6, 0
	v_and_b32_e32 v172, 15, v171
	v_lshrrev_b32_e32 v123, 1, v171
	s_add_i32 s41, s6, 0x20000
	v_mul_u32_u24_e32 v122, 0x50, v172
	v_and_b32_e32 v123, 24, v123
	v_add3_u32 v122, s41, v122, v123
	s_and_b32 s7, s39, 0xc0
	ds_write2_b64 v122, v[130:131], v[4:5] offset1:4
	v_bfe_u32 v4, v171, 2, 4
	s_ashr_i32 s39, s39, 2
	v_mul_u32_u24_e32 v5, 0x50, v4
	v_lshlrev_b32_e32 v123, 4, v171
	s_andn2_b32 s39, s39, 63
	v_lshl_or_b32 v4, s48, 8, v4
	v_and_b32_e32 v146, 48, v123
	v_add_u32_e32 v4, s39, v4
	v_mul_f32_e32 v130, 0x41000000, v170
	v_pk_fma_f32 v[118:119], v[118:119], s[36:37], v[158:159] op_sel_hi:[1,0,1]
	v_pk_fma_f32 v[114:115], v[114:115], s[36:37], v[154:155] op_sel_hi:[1,0,1]
	v_add3_u32 v123, s41, v5, v146
	v_pk_mul_f32 v[118:119], v[130:131], v[118:119] op_sel_hi:[0,1]
	v_pk_mul_f32 v[114:115], v[130:131], v[114:115] op_sel_hi:[0,1]
	v_lshl_add_u32 v128, v4, 10, v146
	v_med3_f32 v5, v118, s70, v164
	v_med3_f32 v118, v114, s70, v164
	v_med3_f32 v119, v119, s70, v164
	v_cvt_pk_fp8_f32 v114, v5, v119
	v_pk_fma_f32 v[120:121], v[120:121], s[36:37], v[156:157] op_sel_hi:[1,0,1]
	v_pk_fma_f32 v[116:117], v[116:117], s[36:37], v[152:153] op_sel_hi:[1,0,1]
	v_pk_mul_f32 v[120:121], v[130:131], v[120:121] op_sel_hi:[0,1]
	v_pk_mul_f32 v[116:117], v[130:131], v[116:117] op_sel_hi:[0,1]
	v_med3_f32 v131, v115, s70, v164
	v_pk_fma_f32 v[110:111], v[110:111], s[36:37], v[150:151] op_sel_hi:[1,0,1]
	v_pk_fma_f32 v[106:107], v[106:107], s[36:37], v[6:7] op_sel_hi:[1,0,1]
	v_med3_f32 v120, v120, s70, v164
	v_med3_f32 v5, v121, s70, v164
	v_pk_mul_f32 v[110:111], v[130:131], v[110:111] op_sel_hi:[0,1]
	v_pk_mul_f32 v[106:107], v[130:131], v[106:107] op_sel_hi:[0,1]
	v_cvt_pk_fp8_f32 v114, v120, v5 op_sel:[0,0,1]
	v_med3_f32 v5, v110, s70, v164
	v_med3_f32 v110, v106, s70, v164
	v_med3_f32 v111, v111, s70, v164
	v_cvt_pk_fp8_f32 v106, v5, v111
	v_pk_fma_f32 v[112:113], v[112:113], s[36:37], v[8:9] op_sel_hi:[1,0,1]
	v_pk_mul_f32 v[112:113], v[130:131], v[112:113] op_sel_hi:[0,1]
	v_med3_f32 v112, v112, s70, v164
	v_med3_f32 v5, v113, s70, v164
	v_cvt_pk_fp8_f32 v106, v112, v5 op_sel:[0,0,1]
	v_mul_f32_e32 v112, 0x41000000, v169
	v_pk_fma_f32 v[102:103], v[102:103], s[36:37], v[158:159] op_sel_hi:[1,0,1]
	v_pk_fma_f32 v[98:99], v[98:99], s[36:37], v[154:155] op_sel_hi:[1,0,1]
	v_cvt_pk_fp8_f32 v115, v118, v131
	v_pk_mul_f32 v[102:103], v[112:113], v[102:103] op_sel_hi:[0,1]
	v_pk_mul_f32 v[98:99], v[112:113], v[98:99] op_sel_hi:[0,1]
	v_med3_f32 v5, v102, s70, v164
	v_med3_f32 v102, v98, s70, v164
	v_med3_f32 v103, v103, s70, v164
	v_cvt_pk_fp8_f32 v98, v5, v103
	v_med3_f32 v116, v116, s70, v164
	v_med3_f32 v117, v117, s70, v164
	v_pk_fma_f32 v[104:105], v[104:105], s[36:37], v[156:157] op_sel_hi:[1,0,1]
	v_pk_fma_f32 v[100:101], v[100:101], s[36:37], v[152:153] op_sel_hi:[1,0,1]
	v_cvt_pk_fp8_f32 v115, v116, v117 op_sel:[0,0,1]
	v_med3_f32 v116, v107, s70, v164
	v_pk_mul_f32 v[104:105], v[112:113], v[104:105] op_sel_hi:[0,1]
	v_pk_mul_f32 v[100:101], v[112:113], v[100:101] op_sel_hi:[0,1]
	v_med3_f32 v113, v99, s70, v164
	v_pk_fma_f32 v[94:95], v[94:95], s[36:37], v[150:151] op_sel_hi:[1,0,1]
	v_pk_fma_f32 v[90:91], v[90:91], s[36:37], v[6:7] op_sel_hi:[1,0,1]
	v_cvt_pk_fp8_f32 v107, v110, v116
	v_med3_f32 v104, v104, s70, v164
	v_med3_f32 v5, v105, s70, v164
	v_pk_mul_f32 v[94:95], v[112:113], v[94:95] op_sel_hi:[0,1]
	v_pk_mul_f32 v[90:91], v[112:113], v[90:91] op_sel_hi:[0,1]
	v_pk_fma_f32 v[108:109], v[108:109], s[36:37], v[2:3] op_sel_hi:[1,0,1]
	v_cvt_pk_fp8_f32 v98, v104, v5 op_sel:[0,0,1]
	v_med3_f32 v5, v94, s70, v164
	v_med3_f32 v94, v90, s70, v164
	v_med3_f32 v95, v95, s70, v164
	s_lshl_b32 s6, s50, 8
	ds_read_b128 v[124:127], v123
	v_pk_mul_f32 v[108:109], v[130:131], v[108:109] op_sel_hi:[0,1]
	v_cvt_pk_fp8_f32 v99, v102, v113
	v_cvt_pk_fp8_f32 v90, v5, v95
	s_or_b32 s6, s7, s6
	v_med3_f32 v108, v108, s70, v164
	v_med3_f32 v109, v109, s70, v164
	v_pk_fma_f32 v[96:97], v[96:97], s[36:37], v[8:9] op_sel_hi:[1,0,1]
	s_ashr_i32 s7, s6, 31
	v_cvt_pk_fp8_f32 v107, v108, v109 op_sel:[0,0,1]
	v_pk_mul_f32 v[96:97], v[112:113], v[96:97] op_sel_hi:[0,1]
	s_add_u32 s86, s16, s6
	s_addc_u32 s87, s17, s7
	v_med3_f32 v100, v100, s70, v164
	v_med3_f32 v101, v101, s70, v164
	v_med3_f32 v96, v96, s70, v164
	v_med3_f32 v5, v97, s70, v164
	v_mov_b32_e32 v108, v128
	v_cvt_pk_fp8_f32 v99, v100, v101 op_sel:[0,0,1]
	v_med3_f32 v100, v91, s70, v164
	v_cvt_pk_fp8_f32 v90, v96, v5 op_sel:[0,0,1]
	v_mul_f32_e32 v96, 0x41000000, v168
	v_pk_fma_f32 v[78:79], v[78:79], s[36:37], v[158:159] op_sel_hi:[1,0,1]
	v_pk_fma_f32 v[74:75], v[74:75], s[36:37], v[154:155] op_sel_hi:[1,0,1]
	s_waitcnt lgkmcnt(0)
	global_store_dwordx4 v108, v[124:127], s[86:87]
	v_cvt_pk_fp8_f32 v91, v94, v100
	v_pk_fma_f32 v[80:81], v[80:81], s[36:37], v[156:157] op_sel_hi:[1,0,1]
	v_pk_mul_f32 v[78:79], v[96:97], v[78:79] op_sel_hi:[0,1]
	v_pk_fma_f32 v[76:77], v[76:77], s[36:37], v[152:153] op_sel_hi:[1,0,1]
	v_pk_mul_f32 v[74:75], v[96:97], v[74:75] op_sel_hi:[0,1]
	ds_write2_b64 v122, v[114:115], v[106:107] offset1:4
	v_or_b32_e32 v110, 16, v4
	v_pk_fma_f32 v[92:93], v[92:93], s[36:37], v[2:3] op_sel_hi:[1,0,1]
	v_pk_mul_f32 v[80:81], v[96:97], v[80:81] op_sel_hi:[0,1]
	v_pk_mul_f32 v[76:77], v[96:97], v[76:77] op_sel_hi:[0,1]
	v_med3_f32 v5, v78, s70, v164
	v_med3_f32 v78, v74, s70, v164
	v_med3_f32 v79, v79, s70, v164
	v_med3_f32 v97, v75, s70, v164
	ds_read_b128 v[106:109], v123
	v_pk_mul_f32 v[92:93], v[112:113], v[92:93] op_sel_hi:[0,1]
	v_cvt_pk_fp8_f32 v74, v5, v79
	v_cvt_pk_fp8_f32 v75, v78, v97
	v_lshl_add_u32 v110, v110, 10, v146
	v_med3_f32 v92, v92, s70, v164
	v_med3_f32 v93, v93, s70, v164
	v_cvt_pk_fp8_f32 v91, v92, v93 op_sel:[0,0,1]
	v_pk_fma_f32 v[62:63], v[62:63], s[36:37], v[150:151] op_sel_hi:[1,0,1]
	v_pk_fma_f32 v[58:59], v[58:59], s[36:37], v[6:7] op_sel_hi:[1,0,1]
	s_add_u32 s86, s16, s6
	s_addc_u32 s87, s17, s7
	v_med3_f32 v80, v80, s70, v164
	v_med3_f32 v76, v76, s70, v164
	v_med3_f32 v5, v81, s70, v164
	v_med3_f32 v77, v77, s70, v164
	v_pk_mul_f32 v[62:63], v[96:97], v[62:63] op_sel_hi:[0,1]
	v_pk_mul_f32 v[58:59], v[96:97], v[58:59] op_sel_hi:[0,1]
	v_mov_b32_e32 v92, v110
	v_cvt_pk_fp8_f32 v74, v80, v5 op_sel:[0,0,1]
	v_cvt_pk_fp8_f32 v75, v76, v77 op_sel:[0,0,1]
	v_med3_f32 v5, v62, s70, v164
	v_med3_f32 v62, v58, s70, v164
	v_med3_f32 v63, v63, s70, v164
	v_med3_f32 v76, v59, s70, v164
	s_waitcnt lgkmcnt(0)
	global_store_dwordx4 v92, v[106:109], s[86:87]
	v_cvt_pk_fp8_f32 v58, v5, v63
	v_cvt_pk_fp8_f32 v59, v62, v76
	ds_write2_b64 v122, v[98:99], v[90:91] offset1:4
	v_or_b32_e32 v94, 32, v4
	v_pk_fma_f32 v[64:65], v[64:65], s[36:37], v[8:9] op_sel_hi:[1,0,1]
	v_pk_fma_f32 v[60:61], v[60:61], s[36:37], v[2:3] op_sel_hi:[1,0,1]
	ds_read_b128 v[90:93], v123
	v_pk_mul_f32 v[64:65], v[96:97], v[64:65] op_sel_hi:[0,1]
	v_pk_mul_f32 v[60:61], v[96:97], v[60:61] op_sel_hi:[0,1]
	v_lshl_add_u32 v94, v94, 10, v146
	v_med3_f32 v64, v64, s70, v164
	v_med3_f32 v60, v60, s70, v164
	v_med3_f32 v5, v65, s70, v164
	v_med3_f32 v61, v61, s70, v164
	v_cvt_pk_fp8_f32 v58, v64, v5 op_sel:[0,0,1]
	v_cvt_pk_fp8_f32 v59, v60, v61 op_sel:[0,0,1]
	s_add_u32 s86, s16, s6
	s_addc_u32 s87, s17, s7
	v_mov_b32_e32 v60, v94
	s_waitcnt lgkmcnt(0)
	global_store_dwordx4 v60, v[90:93], s[86:87]
	ds_write2_b64 v122, v[74:75], v[58:59] offset1:4
	v_mul_f32_e32 v64, 0x41000000, v167
	v_pk_fma_f32 v[74:75], v[86:87], s[36:37], v[158:159] op_sel_hi:[1,0,1]
	v_pk_fma_f32 v[78:79], v[82:83], s[36:37], v[154:155] op_sel_hi:[1,0,1]
	v_pk_mul_f32 v[74:75], v[64:65], v[74:75] op_sel_hi:[0,1]
	v_pk_fma_f32 v[76:77], v[88:89], s[36:37], v[156:157] op_sel_hi:[1,0,1]
	v_pk_fma_f32 v[80:81], v[84:85], s[36:37], v[152:153] op_sel_hi:[1,0,1]
	v_pk_mul_f32 v[78:79], v[64:65], v[78:79] op_sel_hi:[0,1]
	v_med3_f32 v5, v74, s70, v164
	v_med3_f32 v75, v75, s70, v164
	v_pk_mul_f32 v[76:77], v[64:65], v[76:77] op_sel_hi:[0,1]
	v_pk_mul_f32 v[80:81], v[64:65], v[80:81] op_sel_hi:[0,1]
	v_med3_f32 v65, v78, s70, v164
	v_med3_f32 v78, v79, s70, v164
	v_cvt_pk_fp8_f32 v74, v5, v75
	v_cvt_pk_fp8_f32 v75, v65, v78
	v_med3_f32 v79, v80, s70, v164
	v_med3_f32 v65, v81, s70, v164
	v_pk_fma_f32 v[70:71], v[70:71], s[36:37], v[150:151] op_sel_hi:[1,0,1]
	v_pk_fma_f32 v[72:73], v[72:73], s[36:37], v[8:9] op_sel_hi:[1,0,1]
	v_pk_fma_f32 v[66:67], v[66:67], s[36:37], v[6:7] op_sel_hi:[1,0,1]
	v_pk_fma_f32 v[68:69], v[68:69], s[36:37], v[2:3] op_sel_hi:[1,0,1]
	v_med3_f32 v76, v76, s70, v164
	v_med3_f32 v5, v77, s70, v164
	v_cvt_pk_fp8_f32 v75, v79, v65 op_sel:[0,0,1]
	v_pk_mul_f32 v[72:73], v[64:65], v[72:73] op_sel_hi:[0,1]
	v_pk_mul_f32 v[70:71], v[64:65], v[70:71] op_sel_hi:[0,1]
	v_pk_mul_f32 v[68:69], v[64:65], v[68:69] op_sel_hi:[0,1]
	v_pk_mul_f32 v[64:65], v[64:65], v[66:67] op_sel_hi:[0,1]
	v_cvt_pk_fp8_f32 v74, v76, v5 op_sel:[0,0,1]
	v_med3_f32 v5, v70, s70, v164
	v_med3_f32 v66, v64, s70, v164
	v_med3_f32 v67, v71, s70, v164
	v_med3_f32 v70, v65, s70, v164
	v_cvt_pk_fp8_f32 v64, v5, v67
	v_cvt_pk_fp8_f32 v65, v66, v70
	v_or_b32_e32 v62, 48, v4
	ds_read_b128 v[58:61], v123
	v_lshl_add_u32 v62, v62, 10, v146
	v_med3_f32 v71, v72, s70, v164
	v_med3_f32 v68, v68, s70, v164
	v_med3_f32 v5, v73, s70, v164
	v_med3_f32 v66, v69, s70, v164
	v_cvt_pk_fp8_f32 v64, v71, v5 op_sel:[0,0,1]
	v_cvt_pk_fp8_f32 v65, v68, v66 op_sel:[0,0,1]
	s_add_u32 s86, s16, s6
	s_addc_u32 s87, s17, s7
	s_waitcnt lgkmcnt(0)
	global_store_dwordx4 v62, v[58:61], s[86:87]
	ds_write2_b64 v122, v[74:75], v[64:65] offset1:4
	v_mul_f32_e32 v64, 0x41000000, v166
	v_pk_fma_f32 v[54:55], v[54:55], s[36:37], v[158:159] op_sel_hi:[1,0,1]
	v_pk_fma_f32 v[50:51], v[50:51], s[36:37], v[154:155] op_sel_hi:[1,0,1]
	v_pk_mul_f32 v[54:55], v[64:65], v[54:55] op_sel_hi:[0,1]
	v_pk_mul_f32 v[50:51], v[64:65], v[50:51] op_sel_hi:[0,1]
	v_med3_f32 v5, v54, s70, v164
	v_med3_f32 v54, v50, s70, v164
	v_med3_f32 v55, v55, s70, v164
	v_cvt_pk_fp8_f32 v50, v5, v55
	v_pk_fma_f32 v[56:57], v[56:57], s[36:37], v[156:157] op_sel_hi:[1,0,1]
	v_pk_fma_f32 v[52:53], v[52:53], s[36:37], v[152:153] op_sel_hi:[1,0,1]
	v_pk_mul_f32 v[56:57], v[64:65], v[56:57] op_sel_hi:[0,1]
	v_pk_mul_f32 v[52:53], v[64:65], v[52:53] op_sel_hi:[0,1]
	v_med3_f32 v65, v51, s70, v164
	v_pk_fma_f32 v[46:47], v[46:47], s[36:37], v[150:151] op_sel_hi:[1,0,1]
	v_pk_fma_f32 v[42:43], v[42:43], s[36:37], v[6:7] op_sel_hi:[1,0,1]
	v_med3_f32 v56, v56, s70, v164
	v_med3_f32 v5, v57, s70, v164
	v_pk_mul_f32 v[46:47], v[64:65], v[46:47] op_sel_hi:[0,1]
	v_pk_mul_f32 v[42:43], v[64:65], v[42:43] op_sel_hi:[0,1]
	v_cvt_pk_fp8_f32 v50, v56, v5 op_sel:[0,0,1]
	v_med3_f32 v5, v46, s70, v164
	v_med3_f32 v46, v42, s70, v164
	v_med3_f32 v47, v47, s70, v164
	v_cvt_pk_fp8_f32 v42, v5, v47
	v_pk_fma_f32 v[48:49], v[48:49], s[36:37], v[8:9] op_sel_hi:[1,0,1]
	v_pk_mul_f32 v[48:49], v[64:65], v[48:49] op_sel_hi:[0,1]
	v_med3_f32 v48, v48, s70, v164
	v_med3_f32 v5, v49, s70, v164
	v_cvt_pk_fp8_f32 v42, v48, v5 op_sel:[0,0,1]
	v_mul_f32_e32 v48, 0x41000000, v165
	v_pk_fma_f32 v[38:39], v[38:39], s[36:37], v[158:159] op_sel_hi:[1,0,1]
	v_pk_fma_f32 v[34:35], v[34:35], s[36:37], v[154:155] op_sel_hi:[1,0,1]
	v_cvt_pk_fp8_f32 v51, v54, v65
	v_pk_mul_f32 v[38:39], v[48:49], v[38:39] op_sel_hi:[0,1]
	v_pk_mul_f32 v[34:35], v[48:49], v[34:35] op_sel_hi:[0,1]
	v_med3_f32 v5, v38, s70, v164
	v_med3_f32 v38, v34, s70, v164
	v_med3_f32 v39, v39, s70, v164
	v_cvt_pk_fp8_f32 v34, v5, v39
	v_med3_f32 v52, v52, s70, v164
	v_med3_f32 v53, v53, s70, v164
	v_pk_fma_f32 v[40:41], v[40:41], s[36:37], v[156:157] op_sel_hi:[1,0,1]
	v_pk_fma_f32 v[36:37], v[36:37], s[36:37], v[152:153] op_sel_hi:[1,0,1]
	v_cvt_pk_fp8_f32 v51, v52, v53 op_sel:[0,0,1]
	v_med3_f32 v52, v43, s70, v164
	v_pk_mul_f32 v[40:41], v[48:49], v[40:41] op_sel_hi:[0,1]
	v_pk_mul_f32 v[36:37], v[48:49], v[36:37] op_sel_hi:[0,1]
	v_med3_f32 v49, v35, s70, v164
	v_pk_fma_f32 v[30:31], v[30:31], s[36:37], v[150:151] op_sel_hi:[1,0,1]
	v_pk_fma_f32 v[26:27], v[26:27], s[36:37], v[6:7] op_sel_hi:[1,0,1]
	v_cvt_pk_fp8_f32 v43, v46, v52
	v_med3_f32 v40, v40, s70, v164
	v_med3_f32 v5, v41, s70, v164
	v_pk_mul_f32 v[30:31], v[48:49], v[30:31] op_sel_hi:[0,1]
	v_pk_mul_f32 v[26:27], v[48:49], v[26:27] op_sel_hi:[0,1]
	v_add_u32_e32 v62, 0x80, v4
	v_pk_fma_f32 v[44:45], v[44:45], s[36:37], v[2:3] op_sel_hi:[1,0,1]
	v_cvt_pk_fp8_f32 v34, v40, v5 op_sel:[0,0,1]
	v_med3_f32 v5, v30, s70, v164
	v_med3_f32 v30, v26, s70, v164
	v_med3_f32 v31, v31, s70, v164
	ds_read_b128 v[58:61], v123
	v_pk_mul_f32 v[44:45], v[64:65], v[44:45] op_sel_hi:[0,1]
	v_cvt_pk_fp8_f32 v35, v38, v49
	v_cvt_pk_fp8_f32 v26, v5, v31
	v_lshl_add_u32 v62, v62, 10, v146
	v_med3_f32 v44, v44, s70, v164
	v_med3_f32 v45, v45, s70, v164
	v_pk_fma_f32 v[32:33], v[32:33], s[36:37], v[8:9] op_sel_hi:[1,0,1]
	v_cvt_pk_fp8_f32 v43, v44, v45 op_sel:[0,0,1]
	v_pk_mul_f32 v[32:33], v[48:49], v[32:33] op_sel_hi:[0,1]
	s_add_u32 s86, s16, s6
	s_addc_u32 s87, s17, s7
	v_med3_f32 v36, v36, s70, v164
	v_med3_f32 v37, v37, s70, v164
	v_med3_f32 v32, v32, s70, v164
	v_med3_f32 v5, v33, s70, v164
	v_mov_b32_e32 v44, v62
	v_cvt_pk_fp8_f32 v35, v36, v37 op_sel:[0,0,1]
	v_med3_f32 v36, v27, s70, v164
	v_cvt_pk_fp8_f32 v26, v32, v5 op_sel:[0,0,1]
	v_mul_f32_e32 v32, 0x41000000, v1
	v_pk_fma_f32 v[22:23], v[22:23], s[36:37], v[158:159] op_sel_hi:[1,0,1]
	v_pk_fma_f32 v[18:19], v[18:19], s[36:37], v[154:155] op_sel_hi:[1,0,1]
	s_waitcnt lgkmcnt(0)
	global_store_dwordx4 v44, v[58:61], s[86:87]
	v_cvt_pk_fp8_f32 v27, v30, v36
	v_pk_mul_f32 v[22:23], v[32:33], v[22:23] op_sel_hi:[0,1]
	v_pk_mul_f32 v[18:19], v[32:33], v[18:19] op_sel_hi:[0,1]
	ds_write2_b64 v122, v[50:51], v[42:43] offset1:4
	v_add_u32_e32 v46, 0x90, v4
	v_pk_fma_f32 v[28:29], v[28:29], s[36:37], v[2:3] op_sel_hi:[1,0,1]
	v_med3_f32 v1, v22, s70, v164
	v_med3_f32 v5, v18, s70, v164
	v_med3_f32 v22, v23, s70, v164
	v_med3_f32 v23, v19, s70, v164
	ds_read_b128 v[42:45], v123
	v_pk_mul_f32 v[28:29], v[48:49], v[28:29] op_sel_hi:[0,1]
	v_cvt_pk_fp8_f32 v18, v1, v22
	v_cvt_pk_fp8_f32 v19, v5, v23
	v_lshl_add_u32 v46, v46, 10, v146
	v_med3_f32 v28, v28, s70, v164
	v_med3_f32 v29, v29, s70, v164
	v_pk_fma_f32 v[24:25], v[24:25], s[36:37], v[156:157] op_sel_hi:[1,0,1]
	v_pk_fma_f32 v[20:21], v[20:21], s[36:37], v[152:153] op_sel_hi:[1,0,1]
	v_cvt_pk_fp8_f32 v27, v28, v29 op_sel:[0,0,1]
	v_pk_mul_f32 v[24:25], v[32:33], v[24:25] op_sel_hi:[0,1]
	v_pk_mul_f32 v[20:21], v[32:33], v[20:21] op_sel_hi:[0,1]
	v_pk_fma_f32 v[14:15], v[14:15], s[36:37], v[150:151] op_sel_hi:[1,0,1]
	v_pk_fma_f32 v[6:7], v[10:11], s[36:37], v[6:7] op_sel_hi:[1,0,1]
	s_add_u32 s86, s16, s6
	s_addc_u32 s87, s17, s7
	v_med3_f32 v24, v24, s70, v164
	v_med3_f32 v20, v20, s70, v164
	v_med3_f32 v1, v25, s70, v164
	v_med3_f32 v5, v21, s70, v164
	v_pk_mul_f32 v[14:15], v[32:33], v[14:15] op_sel_hi:[0,1]
	v_pk_mul_f32 v[6:7], v[32:33], v[6:7] op_sel_hi:[0,1]
	v_mov_b32_e32 v28, v46
	v_cvt_pk_fp8_f32 v18, v24, v1 op_sel:[0,0,1]
	v_cvt_pk_fp8_f32 v19, v20, v5 op_sel:[0,0,1]
	v_med3_f32 v1, v14, s70, v164
	v_med3_f32 v5, v6, s70, v164
	v_med3_f32 v10, v15, s70, v164
	v_med3_f32 v11, v7, s70, v164
	s_waitcnt lgkmcnt(0)
	global_store_dwordx4 v28, v[42:45], s[86:87]
	v_cvt_pk_fp8_f32 v6, v1, v10
	v_cvt_pk_fp8_f32 v7, v5, v11
	ds_write2_b64 v122, v[34:35], v[26:27] offset1:4
	v_add_u32_e32 v30, 0xa0, v4
	v_pk_fma_f32 v[8:9], v[16:17], s[36:37], v[8:9] op_sel_hi:[1,0,1]
	v_pk_fma_f32 v[2:3], v[12:13], s[36:37], v[2:3] op_sel_hi:[1,0,1]
	ds_read_b128 v[26:29], v123
	v_pk_mul_f32 v[8:9], v[32:33], v[8:9] op_sel_hi:[0,1]
	v_pk_mul_f32 v[2:3], v[32:33], v[2:3] op_sel_hi:[0,1]
	v_lshl_add_u32 v30, v30, 10, v146
	v_med3_f32 v8, v8, s70, v164
	v_med3_f32 v2, v2, s70, v164
	v_med3_f32 v1, v9, s70, v164
	v_med3_f32 v3, v3, s70, v164
	v_cvt_pk_fp8_f32 v6, v8, v1 op_sel:[0,0,1]
	v_cvt_pk_fp8_f32 v7, v2, v3 op_sel:[0,0,1]
	s_add_u32 s86, s16, s6
	s_addc_u32 s87, s17, s7
	v_mov_b32_e32 v2, v30
	s_waitcnt lgkmcnt(0)
	global_store_dwordx4 v2, v[26:29], s[86:87]
	ds_write2_b64 v122, v[18:19], v[6:7] offset1:4
	v_add_u32_e32 v2, 0xb0, v4
	ds_read_b128 v[6:9], v123
	v_ashrrev_i32_e32 v3, 31, v2
	v_lshl_add_u32 v2, v2, 10, v146
	s_add_u32 s86, s16, s6
	s_addc_u32 s87, s17, s7
	s_waitcnt lgkmcnt(0)
	global_store_dwordx4 v2, v[6:9], s[86:87]
	s_and_b64 vcc, exec, s[8:9]
	s_mov_b64 s[6:7], -1
	s_cbranch_vccnz .LBB0_1616
	v_mov_b32_e32 v12, v0
	s_lshl_b32 s7, s40, 8
	v_readfirstlane_b32 s6, v12
	s_and_b32 s8, s6, 0xc0
	s_ashr_i32 s6, s6, 2
	s_andn2_b32 s6, s6, 63
	s_add_i32 s6, s6, s7
	v_and_or_b32 v2, v12, 15, s6
	v_lshlrev_b32_e32 v4, 2, v2
	s_lshl_b64 s[6:7], s[42:43], 11
	s_add_u32 s9, s56, s6
	s_addc_u32 s39, s57, s7
	s_lshl_b32 s6, s38, 8
	global_load_dword v146, v4, s[12:13] offset:0
	global_load_dword v170, v4, s[12:13] offset:64
	global_load_dword v169, v4, s[12:13] offset:128
	global_load_dword v168, v4, s[12:13] offset:192
	global_load_dword v167, v4, s[12:13] offset:512
	global_load_dword v166, v4, s[12:13] offset:576
	global_load_dword v165, v4, s[12:13] offset:640
	global_load_dword v1, v4, s[12:13] offset:704
	s_ashr_i32 s7, s6, 31
	s_lshl_b64 s[6:7], s[6:7], 1
	s_add_u32 s6, s9, s6
	s_addc_u32 s7, s39, s7
	s_lshl_b32 s8, s8, 1
	s_add_u32 s6, s6, s8
	s_addc_u32 s7, s7, 0
	v_and_b32_e32 v2, 48, v12
	global_load_dwordx4 v[6:9], v2, s[6:7]
	s_nop 0
	global_load_dwordx4 v[2:5], v2, s[6:7] offset:64
	s_andn2_b64 vcc, exec, s[14:15]
	s_cbranch_vccnz .LBB0_1615
	s_barrier
	s_branch .LBB0_1615

.LBB0_3348:
	s_mov_b32 s82, 0xc2700000
	v_mov_b32_e32 v190, 0x41898193
	v_lshlrev_b32_e32 v160, 16, v46
	v_and_b32_e32 v161, 0xffff0000, v46
	v_lshlrev_b32_e32 v156, 16, v42
	v_and_b32_e32 v157, 0xffff0000, v42
	v_mul_f32_e32 v42, 0x3d800000, v179
	v_lshlrev_b32_e32 v154, 16, v47
	v_and_b32_e32 v155, 0xffff0000, v47
	v_lshlrev_b32_e32 v46, 16, v44
	v_and_b32_e32 v47, 0xffff0000, v44
	v_lshlrev_b32_e32 v150, 16, v45
	v_and_b32_e32 v151, 0xffff0000, v45
	v_pk_fma_f32 v[44:45], v[42:43], v[130:131], v[160:161] op_sel_hi:[0,1,1]
	v_med3_f32 v44, v44, s82, v190
	v_med3_f32 v45, v45, s82, v190
	v_exp_f32_e64 v130, -v44
	v_exp_f32_e64 v131, -v45
	v_pk_fma_f32 v[132:133], v[42:43], v[132:133], v[154:155] op_sel_hi:[0,1,1]
	v_med3_f32 v132, v132, s82, v190
	v_med3_f32 v133, v133, s82, v190
	v_pk_add_f32 v[130:131], v[130:131], 1.0 op_sel_hi:[1,0]
	v_exp_f32_e64 v188, -v132
	v_exp_f32_e64 v189, -v133
	v_lshlrev_b32_e32 v152, 16, v48
	v_and_b32_e32 v153, 0xffff0000, v48
	v_pk_add_f32 v[188:189], v[188:189], 1.0 op_sel_hi:[1,0]
	v_pk_fma_f32 v[122:123], v[42:43], v[122:123], v[152:153] op_sel_hi:[0,1,1]
	v_pk_mul_f32 v[184:185], v[130:131], v[188:189]
	v_rcp_f32_e32 v184, v184
	v_rcp_f32_e32 v185, v185
	s_nop 0
	v_pk_mul_f32 v[186:187], v[184:185], v[188:189]
	v_pk_mul_f32 v[188:189], v[184:185], v[130:131]
	v_pk_mul_f32 v[44:45], v[44:45], v[186:187]
	v_med3_f32 v122, v122, s82, v190
	v_med3_f32 v123, v123, s82, v190
	v_lshlrev_b32_e32 v48, 16, v49
	v_pk_mul_f32 v[130:131], v[132:133], v[188:189]
	v_exp_f32_e64 v132, -v122
	v_exp_f32_e64 v133, -v123
	v_and_b32_e32 v49, 0xffff0000, v49
	v_pk_fma_f32 v[124:125], v[42:43], v[124:125], v[48:49] op_sel_hi:[0,1,1]
	v_lshlrev_b32_e32 v158, 16, v43
	v_and_b32_e32 v159, 0xffff0000, v43
	v_med3_f32 v124, v124, s82, v190
	v_med3_f32 v125, v125, s82, v190
	v_pk_fma_f32 v[136:137], v[42:43], v[136:137], v[158:159] op_sel_hi:[0,1,1]
	v_pk_fma_f32 v[134:135], v[42:43], v[134:135], v[156:157] op_sel_hi:[0,1,1]
	v_pk_fma_f32 v[128:129], v[42:43], v[128:129], v[150:151] op_sel_hi:[0,1,1]
	v_pk_add_f32 v[132:133], v[132:133], 1.0 op_sel_hi:[1,0]
	v_pk_fma_f32 v[42:43], v[42:43], v[126:127], v[46:47] op_sel_hi:[0,1,1]
	v_exp_f32_e64 v188, -v124
	v_exp_f32_e64 v189, -v125
	v_med3_f32 v42, v42, s81, v170
	v_pk_add_f32 v[188:189], v[188:189], 1.0 op_sel_hi:[1,0]
	v_med3_f32 v43, v43, s81, v170
	v_pk_mul_f32 v[184:185], v[132:133], v[188:189]
	v_rcp_f32_e32 v184, v184
	v_rcp_f32_e32 v185, v185
	s_nop 0
	v_pk_mul_f32 v[186:187], v[184:185], v[188:189]
	v_pk_mul_f32 v[188:189], v[184:185], v[132:133]
	v_pk_mul_f32 v[122:123], v[122:123], v[186:187]
	v_pk_mul_f32 v[42:43], v[122:123], v[42:43]
	v_med3_f32 v123, v129, s81, v170
	v_cvt_pk_fp8_f32 v129, v42, v43
	v_med3_f32 v122, v128, s81, v170
	v_pk_mul_f32 v[42:43], v[124:125], v[188:189]
	v_med3_f32 v134, v134, s81, v170
	v_med3_f32 v135, v135, s81, v170
	v_pk_mul_f32 v[42:43], v[42:43], v[122:123]
	v_pk_mul_f32 v[44:45], v[44:45], v[134:135]
	v_cvt_pk_fp8_f32 v129, v42, v43 op_sel:[0,0,1]
	v_mul_f32_e32 v42, 0x3d800000, v178
	v_cvt_pk_fp8_f32 v128, v44, v45
	v_pk_fma_f32 v[44:45], v[42:43], v[114:115], v[160:161] op_sel_hi:[0,1,1]
	v_med3_f32 v44, v44, s82, v190
	v_med3_f32 v45, v45, s82, v190
	v_exp_f32_e64 v114, -v44
	v_exp_f32_e64 v115, -v45
	v_pk_fma_f32 v[116:117], v[42:43], v[116:117], v[154:155] op_sel_hi:[0,1,1]
	v_med3_f32 v116, v116, s82, v190
	v_med3_f32 v117, v117, s82, v190
	v_pk_add_f32 v[114:115], v[114:115], 1.0 op_sel_hi:[1,0]
	v_exp_f32_e64 v188, -v116
	v_exp_f32_e64 v189, -v117
	v_pk_fma_f32 v[106:107], v[42:43], v[106:107], v[152:153] op_sel_hi:[0,1,1]
	v_med3_f32 v106, v106, s82, v190
	v_pk_add_f32 v[188:189], v[188:189], 1.0 op_sel_hi:[1,0]
	v_med3_f32 v107, v107, s82, v190
	v_pk_mul_f32 v[184:185], v[114:115], v[188:189]
	v_rcp_f32_e32 v184, v184
	v_rcp_f32_e32 v185, v185
	s_nop 0
	v_pk_mul_f32 v[186:187], v[184:185], v[188:189]
	v_pk_mul_f32 v[188:189], v[184:185], v[114:115]
	v_pk_mul_f32 v[44:45], v[44:45], v[186:187]
	v_pk_fma_f32 v[108:109], v[42:43], v[108:109], v[48:49] op_sel_hi:[0,1,1]
	v_med3_f32 v108, v108, s82, v190
	v_med3_f32 v109, v109, s82, v190
	v_pk_mul_f32 v[114:115], v[116:117], v[188:189]
	v_exp_f32_e64 v116, -v106
	v_exp_f32_e64 v117, -v107
	v_pk_fma_f32 v[120:121], v[42:43], v[120:121], v[158:159] op_sel_hi:[0,1,1]
	v_pk_fma_f32 v[118:119], v[42:43], v[118:119], v[156:157] op_sel_hi:[0,1,1]
	v_pk_fma_f32 v[112:113], v[42:43], v[112:113], v[150:151] op_sel_hi:[0,1,1]
	v_pk_add_f32 v[116:117], v[116:117], 1.0 op_sel_hi:[1,0]
	v_pk_fma_f32 v[42:43], v[42:43], v[110:111], v[46:47] op_sel_hi:[0,1,1]
	v_exp_f32_e64 v188, -v108
	v_exp_f32_e64 v189, -v109
	v_med3_f32 v118, v118, s81, v170
	v_pk_add_f32 v[188:189], v[188:189], 1.0 op_sel_hi:[1,0]
	v_med3_f32 v119, v119, s81, v170
	v_med3_f32 v42, v42, s81, v170
	v_med3_f32 v43, v43, s81, v170
	v_pk_mul_f32 v[184:185], v[116:117], v[188:189]
	v_rcp_f32_e32 v184, v184
	v_rcp_f32_e32 v185, v185
	s_nop 0
	v_pk_mul_f32 v[186:187], v[184:185], v[188:189]
	v_pk_mul_f32 v[188:189], v[184:185], v[116:117]
	v_pk_mul_f32 v[106:107], v[106:107], v[186:187]
	v_pk_mul_f32 v[44:45], v[44:45], v[118:119]
	v_pk_mul_f32 v[42:43], v[106:107], v[42:43]
	v_med3_f32 v106, v112, s81, v170
	v_med3_f32 v107, v113, s81, v170
	v_mov_b32_e32 v142, v0
	v_cvt_pk_fp8_f32 v112, v44, v45
	v_cvt_pk_fp8_f32 v113, v42, v43
	v_med3_f32 v134, v136, s81, v170
	v_readfirstlane_b32 s65, v142
	v_med3_f32 v135, v137, s81, v170
	s_ashr_i32 s10, s65, 6
	v_pk_mul_f32 v[130:131], v[130:131], v[134:135]
	v_med3_f32 v118, v120, s81, v170
	v_med3_f32 v119, v121, s81, v170
	v_pk_mul_f32 v[42:43], v[108:109], v[188:189]
	s_mul_i32 s11, s10, 0xb00
	v_cvt_pk_fp8_f32 v128, v130, v131 op_sel:[0,0,1]
	v_pk_mul_f32 v[114:115], v[114:115], v[118:119]
	v_pk_mul_f32 v[42:43], v[42:43], v[106:107]
	s_add_i32 s67, s11, 0
	v_and_b32_e32 v147, 15, v142
	v_lshrrev_b32_e32 v125, 1, v142
	v_cvt_pk_fp8_f32 v112, v114, v115 op_sel:[0,0,1]
	v_cvt_pk_fp8_f32 v113, v42, v43 op_sel:[0,0,1]
	s_add_i32 s67, s67, 0x20000
	v_mul_u32_u24_e32 v124, 48, v147
	v_and_b32_e32 v42, 24, v125
	v_add3_u32 v108, s67, v124, v42
	ds_write_b64 v108, v[128:129]
	ds_write_b64 v108, v[112:113] offset:768
	v_mul_f32_e32 v112, 0x3d800000, v177
	v_pk_fma_f32 v[98:99], v[112:113], v[98:99], v[160:161] op_sel_hi:[0,1,1]
	v_med3_f32 v98, v98, s82, v190
	v_med3_f32 v99, v99, s82, v190
	v_exp_f32_e64 v114, -v98
	v_exp_f32_e64 v115, -v99
	v_pk_fma_f32 v[100:101], v[112:113], v[100:101], v[154:155] op_sel_hi:[0,1,1]
	v_med3_f32 v100, v100, s82, v190
	v_med3_f32 v101, v101, s82, v190
	v_pk_add_f32 v[114:115], v[114:115], 1.0 op_sel_hi:[1,0]
	v_exp_f32_e64 v188, -v100
	v_exp_f32_e64 v189, -v101
	v_pk_fma_f32 v[102:103], v[112:113], v[102:103], v[156:157] op_sel_hi:[0,1,1]
	v_pk_fma_f32 v[90:91], v[112:113], v[90:91], v[152:153] op_sel_hi:[0,1,1]
	v_pk_add_f32 v[188:189], v[188:189], 1.0 op_sel_hi:[1,0]
	v_pk_fma_f32 v[104:105], v[112:113], v[104:105], v[158:159] op_sel_hi:[0,1,1]
	v_med3_f32 v102, v102, s81, v170
	v_med3_f32 v103, v103, s81, v170
	v_pk_mul_f32 v[184:185], v[114:115], v[188:189]
	v_rcp_f32_e32 v184, v184
	v_rcp_f32_e32 v185, v185
	s_nop 0
	v_pk_mul_f32 v[186:187], v[184:185], v[188:189]
	v_pk_mul_f32 v[188:189], v[184:185], v[114:115]
	v_pk_mul_f32 v[98:99], v[98:99], v[186:187]
	v_med3_f32 v90, v90, s82, v190
	v_med3_f32 v91, v91, s82, v190
	v_pk_mul_f32 v[98:99], v[98:99], v[102:103]
	v_med3_f32 v102, v104, s81, v170
	v_med3_f32 v103, v105, s81, v170
	v_exp_f32_e64 v104, -v90
	v_exp_f32_e64 v105, -v91
	v_pk_mul_f32 v[100:101], v[100:101], v[188:189]
	v_pk_fma_f32 v[92:93], v[112:113], v[92:93], v[48:49] op_sel_hi:[0,1,1]
	v_pk_mul_f32 v[100:101], v[100:101], v[102:103]
	v_pk_add_f32 v[102:103], v[104:105], 1.0 op_sel_hi:[1,0]
	v_med3_f32 v92, v92, s82, v190
	v_rcp_f32_e32 v102, v102
	v_rcp_f32_e32 v103, v103
	v_med3_f32 v93, v93, s82, v190
	v_pk_fma_f32 v[94:95], v[112:113], v[94:95], v[46:47] op_sel_hi:[0,1,1]
	v_pk_fma_f32 v[96:97], v[112:113], v[96:97], v[150:151] op_sel_hi:[0,1,1]
	v_pk_mul_f32 v[90:91], v[90:91], v[102:103]
	v_exp_f32_e64 v102, -v92
	v_exp_f32_e64 v103, -v93
	v_med3_f32 v94, v94, s81, v170
	v_med3_f32 v95, v95, s81, v170
	v_pk_mul_f32 v[90:91], v[90:91], v[94:95]
	v_med3_f32 v94, v96, s81, v170
	v_med3_f32 v95, v97, s81, v170
	v_pk_add_f32 v[96:97], v[102:103], 1.0 op_sel_hi:[1,0]
	v_rcp_f32_e32 v96, v96
	v_rcp_f32_e32 v97, v97
	v_cvt_pk_fp8_f32 v103, v90, v91
	v_bfe_u32 v106, v142, 1, 5
	v_pk_mul_f32 v[90:91], v[92:93], v[96:97]
	v_lshlrev_b32_e32 v43, 4, v142
	v_pk_mul_f32 v[90:91], v[90:91], v[94:95]
	s_ashr_i32 s65, s65, 2
	v_cvt_pk_fp8_f32 v103, v90, v91 op_sel:[0,0,1]
	v_mul_f32_e32 v90, 0x3d800000, v176
	v_pk_fma_f32 v[82:83], v[90:91], v[82:83], v[160:161] op_sel_hi:[0,1,1]
	v_med3_f32 v82, v82, s82, v190
	v_med3_f32 v83, v83, s82, v190
	v_exp_f32_e64 v92, -v82
	v_exp_f32_e64 v93, -v83
	v_pk_fma_f32 v[84:85], v[90:91], v[84:85], v[154:155] op_sel_hi:[0,1,1]
	v_med3_f32 v84, v84, s82, v190
	v_med3_f32 v85, v85, s82, v190
	v_pk_add_f32 v[92:93], v[92:93], 1.0 op_sel_hi:[1,0]
	v_exp_f32_e64 v188, -v84
	v_exp_f32_e64 v189, -v85
	v_pk_fma_f32 v[86:87], v[90:91], v[86:87], v[156:157] op_sel_hi:[0,1,1]
	v_pk_fma_f32 v[66:67], v[90:91], v[66:67], v[152:153] op_sel_hi:[0,1,1]
	v_pk_add_f32 v[188:189], v[188:189], 1.0 op_sel_hi:[1,0]
	v_pk_fma_f32 v[88:89], v[90:91], v[88:89], v[158:159] op_sel_hi:[0,1,1]
	v_med3_f32 v86, v86, s81, v170
	v_med3_f32 v87, v87, s81, v170
	v_pk_mul_f32 v[184:185], v[92:93], v[188:189]
	v_rcp_f32_e32 v184, v184
	v_rcp_f32_e32 v185, v185
	s_nop 0
	v_pk_mul_f32 v[186:187], v[184:185], v[188:189]
	v_pk_mul_f32 v[188:189], v[184:185], v[92:93]
	v_pk_mul_f32 v[82:83], v[82:83], v[186:187]
	v_med3_f32 v66, v66, s82, v190
	v_med3_f32 v67, v67, s82, v190
	v_pk_mul_f32 v[82:83], v[82:83], v[86:87]
	v_med3_f32 v86, v88, s81, v170
	v_med3_f32 v87, v89, s81, v170
	v_exp_f32_e64 v88, -v66
	v_exp_f32_e64 v89, -v67
	v_pk_mul_f32 v[84:85], v[84:85], v[188:189]
	v_pk_fma_f32 v[68:69], v[90:91], v[68:69], v[48:49] op_sel_hi:[0,1,1]
	v_pk_mul_f32 v[84:85], v[84:85], v[86:87]
	v_pk_add_f32 v[86:87], v[88:89], 1.0 op_sel_hi:[1,0]
	v_med3_f32 v68, v68, s82, v190
	v_rcp_f32_e32 v86, v86
	v_rcp_f32_e32 v87, v87
	v_med3_f32 v69, v69, s82, v190
	v_pk_fma_f32 v[74:75], v[90:91], v[74:75], v[46:47] op_sel_hi:[0,1,1]
	v_pk_fma_f32 v[76:77], v[90:91], v[76:77], v[150:151] op_sel_hi:[0,1,1]
	v_pk_mul_f32 v[66:67], v[66:67], v[86:87]
	v_exp_f32_e64 v86, -v68
	v_exp_f32_e64 v87, -v69
	v_med3_f32 v74, v74, s81, v170
	v_med3_f32 v75, v75, s81, v170
	v_pk_mul_f32 v[66:67], v[66:67], v[74:75]
	v_med3_f32 v74, v76, s81, v170
	v_med3_f32 v75, v77, s81, v170
	v_pk_add_f32 v[76:77], v[86:87], 1.0 op_sel_hi:[1,0]
	v_rcp_f32_e32 v76, v76
	v_rcp_f32_e32 v77, v77
	v_cvt_pk_fp8_f32 v87, v66, v67
	v_cvt_pk_fp8_f32 v102, v98, v99
	v_pk_mul_f32 v[66:67], v[68:69], v[76:77]
	v_mul_f32_e32 v68, 0x3d800000, v175
	v_pk_fma_f32 v[70:71], v[68:69], v[70:71], v[160:161] op_sel_hi:[0,1,1]
	v_med3_f32 v70, v70, s82, v190
	v_med3_f32 v71, v71, s82, v190
	v_pk_mul_f32 v[66:67], v[66:67], v[74:75]
	v_exp_f32_e64 v74, -v70
	v_exp_f32_e64 v75, -v71
	v_pk_fma_f32 v[72:73], v[68:69], v[72:73], v[154:155] op_sel_hi:[0,1,1]
	v_med3_f32 v72, v72, s82, v190
	v_med3_f32 v73, v73, s82, v190
	v_pk_add_f32 v[74:75], v[74:75], 1.0 op_sel_hi:[1,0]
	v_pk_fma_f32 v[76:77], v[68:69], v[80:81], v[158:159] op_sel_hi:[0,1,1]
	v_exp_f32_e64 v188, -v72
	v_exp_f32_e64 v189, -v73
	v_pk_fma_f32 v[58:59], v[68:69], v[58:59], v[152:153] op_sel_hi:[0,1,1]
	v_med3_f32 v58, v58, s82, v190
	v_pk_add_f32 v[188:189], v[188:189], 1.0 op_sel_hi:[1,0]
	v_med3_f32 v59, v59, s82, v190
	v_pk_mul_f32 v[184:185], v[74:75], v[188:189]
	v_rcp_f32_e32 v184, v184
	v_rcp_f32_e32 v185, v185
	s_nop 0
	v_pk_mul_f32 v[186:187], v[184:185], v[188:189]
	v_pk_mul_f32 v[188:189], v[184:185], v[74:75]
	v_pk_mul_f32 v[70:71], v[70:71], v[186:187]
	v_pk_fma_f32 v[60:61], v[68:69], v[60:61], v[48:49] op_sel_hi:[0,1,1]
	v_med3_f32 v60, v60, s82, v190
	v_med3_f32 v61, v61, s82, v190
	v_pk_mul_f32 v[72:73], v[72:73], v[188:189]
	v_exp_f32_e64 v74, -v58
	v_exp_f32_e64 v75, -v59
	v_pk_fma_f32 v[78:79], v[68:69], v[78:79], v[156:157] op_sel_hi:[0,1,1]
	v_pk_fma_f32 v[64:65], v[68:69], v[64:65], v[150:151] op_sel_hi:[0,1,1]
	v_pk_fma_f32 v[62:63], v[68:69], v[62:63], v[46:47] op_sel_hi:[0,1,1]
	v_pk_add_f32 v[74:75], v[74:75], 1.0 op_sel_hi:[1,0]
	v_exp_f32_e64 v188, -v60
	v_exp_f32_e64 v189, -v61
	v_med3_f32 v62, v62, s81, v170
	v_med3_f32 v63, v63, s81, v170
	v_mul_u32_u24_e32 v42, 48, v106
	v_pk_mul_f32 v[58:59], v[58:59], v[62:63]
	v_med3_f32 v62, v64, s81, v170
	v_med3_f32 v63, v65, s81, v170
	v_pk_add_f32 v[188:189], v[188:189], 1.0 op_sel_hi:[1,0]
	v_pk_mul_f32 v[184:185], v[74:75], v[188:189]
	v_rcp_f32_e32 v184, v184
	v_rcp_f32_e32 v185, v185
	s_nop 0
	v_pk_mul_f32 v[186:187], v[184:185], v[188:189]
	v_pk_mul_f32 v[188:189], v[184:185], v[74:75]
	v_pk_mul_f32 v[58:59], v[58:59], v[186:187]
	v_cvt_pk_fp8_f32 v69, v58, v59
	v_and_b32_e32 v142, 16, v43
	s_andn2_b32 s65, s65, 63
	v_pk_mul_f32 v[58:59], v[60:61], v[188:189]
	v_lshl_or_b32 v106, s74, 8, v106
	v_pk_mul_f32 v[58:59], v[58:59], v[62:63]
	v_cvt_pk_fp8_f32 v86, v82, v83
	v_cvt_pk_fp8_f32 v69, v58, v59 op_sel:[0,0,1]
	v_mul_f32_e32 v58, 0x3d800000, v174
	v_pk_fma_f32 v[50:51], v[58:59], v[50:51], v[160:161] op_sel_hi:[0,1,1]
	v_med3_f32 v50, v50, s82, v190
	v_med3_f32 v51, v51, s82, v190
	v_exp_f32_e64 v60, -v50
	v_exp_f32_e64 v61, -v51
	v_pk_fma_f32 v[52:53], v[58:59], v[52:53], v[154:155] op_sel_hi:[0,1,1]
	v_med3_f32 v52, v52, s82, v190
	v_med3_f32 v53, v53, s82, v190
	v_pk_add_f32 v[60:61], v[60:61], 1.0 op_sel_hi:[1,0]
	v_exp_f32_e64 v188, -v52
	v_exp_f32_e64 v189, -v53
	v_pk_fma_f32 v[54:55], v[58:59], v[54:55], v[156:157] op_sel_hi:[0,1,1]
	v_pk_fma_f32 v[34:35], v[58:59], v[34:35], v[152:153] op_sel_hi:[0,1,1]
	v_pk_add_f32 v[188:189], v[188:189], 1.0 op_sel_hi:[1,0]
	v_pk_fma_f32 v[56:57], v[58:59], v[56:57], v[158:159] op_sel_hi:[0,1,1]
	v_med3_f32 v54, v54, s81, v170
	v_med3_f32 v55, v55, s81, v170
	v_pk_mul_f32 v[184:185], v[60:61], v[188:189]
	v_rcp_f32_e32 v184, v184
	v_rcp_f32_e32 v185, v185
	s_nop 0
	v_pk_mul_f32 v[186:187], v[184:185], v[188:189]
	v_pk_mul_f32 v[188:189], v[184:185], v[60:61]
	v_pk_mul_f32 v[50:51], v[50:51], v[186:187]
	v_med3_f32 v34, v34, s82, v190
	v_med3_f32 v35, v35, s82, v190
	v_pk_mul_f32 v[50:51], v[50:51], v[54:55]
	v_med3_f32 v54, v56, s81, v170
	v_med3_f32 v55, v57, s81, v170
	v_exp_f32_e64 v56, -v34
	v_exp_f32_e64 v57, -v35
	v_pk_mul_f32 v[52:53], v[52:53], v[188:189]
	v_pk_fma_f32 v[36:37], v[58:59], v[36:37], v[48:49] op_sel_hi:[0,1,1]
	v_pk_mul_f32 v[52:53], v[52:53], v[54:55]
	v_pk_add_f32 v[54:55], v[56:57], 1.0 op_sel_hi:[1,0]
	v_med3_f32 v36, v36, s82, v190
	v_med3_f32 v37, v37, s82, v190
	s_lshl_b32 s10, s10, 5
	v_add3_u32 v109, s67, v42, v142
	v_add_u32_e32 v106, s65, v106
	v_exp_f32_e64 v188, -v36
	v_exp_f32_e64 v189, -v37
	s_lshl_b32 s11, s76, 7
	s_and_b32 s10, s10, 0x60
	ds_read_b128 v[42:45], v109
	s_or_b32 s10, s10, s11
	v_lshl_add_u32 v110, v106, 10, v142
	v_cvt_pk_fp8_f32 v102, v100, v101 op_sel:[0,0,1]
	v_pk_fma_f32 v[38:39], v[58:59], v[38:39], v[46:47] op_sel_hi:[0,1,1]
	s_ashr_i32 s11, s10, 31
	v_cvt_pk_fp8_f32 v86, v84, v85 op_sel:[0,0,1]
	v_cvt_pk_fp8_f32 v87, v66, v67 op_sel:[0,0,1]
	v_pk_fma_f32 v[40:41], v[58:59], v[40:41], v[150:151] op_sel_hi:[0,1,1]
	v_med3_f32 v38, v38, s81, v170
	v_med3_f32 v39, v39, s81, v170
	s_add_u32 s86, s18, s10
	s_addc_u32 s87, s19, s11
	v_pk_mul_f32 v[34:35], v[34:35], v[38:39]
	v_med3_f32 v38, v40, s81, v170
	v_med3_f32 v39, v41, s81, v170
	v_pk_add_f32 v[188:189], v[188:189], 1.0 op_sel_hi:[1,0]
	v_mov_b32_e32 v66, v110
	v_pk_mul_f32 v[184:185], v[54:55], v[188:189]
	v_rcp_f32_e32 v184, v184
	v_rcp_f32_e32 v185, v185
	s_nop 0
	v_pk_mul_f32 v[186:187], v[184:185], v[188:189]
	v_pk_mul_f32 v[188:189], v[184:185], v[54:55]
	v_pk_mul_f32 v[34:35], v[34:35], v[186:187]
	s_waitcnt lgkmcnt(0)
	global_store_dwordx4 v66, v[42:45], s[86:87]
	ds_write_b64 v108, v[102:103]
	ds_write_b64 v108, v[86:87] offset:768
	v_or_b32_e32 v66, 32, v106
	ds_read_b128 v[42:45], v109
	v_ashrrev_i32_e32 v67, 31, v66
	v_cvt_pk_fp8_f32 v55, v34, v35
	v_lshl_add_u32 v66, v66, 10, v142
	v_pk_mul_f32 v[34:35], v[36:37], v[188:189]
	v_mul_f32_e32 v40, 0x3d800000, v171
	s_add_u32 s86, s18, s10
	s_addc_u32 s87, s19, s11
	v_pk_mul_f32 v[34:35], v[34:35], v[38:39]
	v_pk_fma_f32 v[26:27], v[40:41], v[26:27], v[160:161] op_sel_hi:[0,1,1]
	v_cvt_pk_fp8_f32 v55, v34, v35 op_sel:[0,0,1]
	v_mov_b32_e32 v34, v66
	v_med3_f32 v26, v26, s82, v190
	v_med3_f32 v27, v27, s82, v190
	s_waitcnt lgkmcnt(0)
	global_store_dwordx4 v34, v[42:45], s[86:87]
	v_pk_fma_f32 v[28:29], v[40:41], v[28:29], v[154:155] op_sel_hi:[0,1,1]
	v_med3_f32 v28, v28, s82, v190
	v_exp_f32_e64 v42, -v26
	v_exp_f32_e64 v43, -v27
	v_med3_f32 v29, v29, s82, v190
	v_exp_f32_e64 v188, -v28
	v_exp_f32_e64 v189, -v29
	v_pk_add_f32 v[42:43], v[42:43], 1.0 op_sel_hi:[1,0]
	v_pk_fma_f32 v[30:31], v[40:41], v[30:31], v[156:157] op_sel_hi:[0,1,1]
	v_pk_fma_f32 v[18:19], v[40:41], v[18:19], v[152:153] op_sel_hi:[0,1,1]
	v_pk_fma_f32 v[32:33], v[40:41], v[32:33], v[158:159] op_sel_hi:[0,1,1]
	v_med3_f32 v30, v30, s81, v170
	v_pk_add_f32 v[188:189], v[188:189], 1.0 op_sel_hi:[1,0]
	v_med3_f32 v31, v31, s81, v170
	v_pk_mul_f32 v[184:185], v[42:43], v[188:189]
	v_rcp_f32_e32 v184, v184
	v_rcp_f32_e32 v185, v185
	s_nop 0
	v_pk_mul_f32 v[186:187], v[184:185], v[188:189]
	v_pk_mul_f32 v[188:189], v[184:185], v[42:43]
	v_pk_mul_f32 v[26:27], v[26:27], v[186:187]
	v_med3_f32 v18, v18, s82, v190
	v_med3_f32 v19, v19, s82, v190
	v_pk_mul_f32 v[26:27], v[26:27], v[30:31]
	v_med3_f32 v30, v32, s81, v170
	v_med3_f32 v31, v33, s81, v170
	v_exp_f32_e64 v32, -v18
	v_exp_f32_e64 v33, -v19
	v_pk_mul_f32 v[28:29], v[28:29], v[188:189]
	v_pk_fma_f32 v[20:21], v[40:41], v[20:21], v[48:49] op_sel_hi:[0,1,1]
	v_pk_mul_f32 v[28:29], v[28:29], v[30:31]
	v_pk_add_f32 v[30:31], v[32:33], 1.0 op_sel_hi:[1,0]
	v_med3_f32 v20, v20, s82, v190
	v_rcp_f32_e32 v30, v30
	v_rcp_f32_e32 v31, v31
	v_med3_f32 v21, v21, s82, v190
	v_pk_fma_f32 v[22:23], v[40:41], v[22:23], v[46:47] op_sel_hi:[0,1,1]
	v_pk_fma_f32 v[24:25], v[40:41], v[24:25], v[150:151] op_sel_hi:[0,1,1]
	v_pk_mul_f32 v[18:19], v[18:19], v[30:31]
	v_exp_f32_e64 v30, -v20
	v_exp_f32_e64 v31, -v21
	v_med3_f32 v22, v22, s81, v170
	v_med3_f32 v23, v23, s81, v170
	v_pk_mul_f32 v[18:19], v[18:19], v[22:23]
	v_med3_f32 v22, v24, s81, v170
	v_med3_f32 v23, v25, s81, v170
	v_pk_add_f32 v[24:25], v[30:31], 1.0 op_sel_hi:[1,0]
	v_rcp_f32_e32 v24, v24
	v_rcp_f32_e32 v25, v25
	v_cvt_pk_fp8_f32 v31, v18, v19
	v_med3_f32 v78, v78, s81, v170
	v_med3_f32 v79, v79, s81, v170
	v_pk_mul_f32 v[18:19], v[20:21], v[24:25]
	v_pk_mul_f32 v[70:71], v[70:71], v[78:79]
	v_pk_mul_f32 v[18:19], v[18:19], v[22:23]
	v_cvt_pk_fp8_f32 v31, v18, v19 op_sel:[0,0,1]
	v_mul_f32_e32 v18, 0x3d800000, v169
	v_pk_fma_f32 v[10:11], v[18:19], v[10:11], v[160:161] op_sel_hi:[0,1,1]
	v_med3_f32 v10, v10, s82, v190
	v_med3_f32 v11, v11, s82, v190
	v_exp_f32_e64 v20, -v10
	v_exp_f32_e64 v21, -v11
	v_pk_fma_f32 v[12:13], v[18:19], v[12:13], v[154:155] op_sel_hi:[0,1,1]
	v_med3_f32 v12, v12, s82, v190
	v_med3_f32 v13, v13, s82, v190
	v_pk_add_f32 v[20:21], v[20:21], 1.0 op_sel_hi:[1,0]
	v_exp_f32_e64 v188, -v12
	v_exp_f32_e64 v189, -v13
	v_pk_fma_f32 v[14:15], v[18:19], v[14:15], v[156:157] op_sel_hi:[0,1,1]
	v_pk_fma_f32 v[2:3], v[18:19], v[2:3], v[152:153] op_sel_hi:[0,1,1]
	v_pk_add_f32 v[188:189], v[188:189], 1.0 op_sel_hi:[1,0]
	v_pk_fma_f32 v[16:17], v[18:19], v[16:17], v[158:159] op_sel_hi:[0,1,1]
	v_med3_f32 v14, v14, s81, v170
	v_med3_f32 v15, v15, s81, v170
	v_pk_mul_f32 v[184:185], v[20:21], v[188:189]
	v_rcp_f32_e32 v184, v184
	v_rcp_f32_e32 v185, v185
	s_nop 0
	v_pk_mul_f32 v[186:187], v[184:185], v[188:189]
	v_pk_mul_f32 v[188:189], v[184:185], v[20:21]
	v_pk_mul_f32 v[10:11], v[10:11], v[186:187]
	v_med3_f32 v2, v2, s82, v190
	v_med3_f32 v3, v3, s82, v190
	v_pk_mul_f32 v[10:11], v[10:11], v[14:15]
	v_med3_f32 v14, v16, s81, v170
	v_med3_f32 v15, v17, s81, v170
	v_exp_f32_e64 v16, -v2
	v_exp_f32_e64 v17, -v3
	v_pk_mul_f32 v[12:13], v[12:13], v[188:189]
	v_pk_fma_f32 v[4:5], v[18:19], v[4:5], v[48:49] op_sel_hi:[0,1,1]
	v_pk_mul_f32 v[12:13], v[12:13], v[14:15]
	v_pk_add_f32 v[14:15], v[16:17], 1.0 op_sel_hi:[1,0]
	v_med3_f32 v4, v4, s82, v190
	v_med3_f32 v5, v5, s82, v190
	v_cvt_pk_fp8_f32 v68, v70, v71
	v_exp_f32_e64 v188, -v4
	v_exp_f32_e64 v189, -v5
	v_cvt_pk_fp8_f32 v54, v50, v51
	v_med3_f32 v76, v76, s81, v170
	v_med3_f32 v77, v77, s81, v170
	v_pk_fma_f32 v[6:7], v[18:19], v[6:7], v[46:47] op_sel_hi:[0,1,1]
	v_pk_mul_f32 v[72:73], v[72:73], v[76:77]
	v_pk_fma_f32 v[8:9], v[18:19], v[8:9], v[150:151] op_sel_hi:[0,1,1]
	v_med3_f32 v6, v6, s81, v170
	v_med3_f32 v7, v7, s81, v170
	v_cvt_pk_fp8_f32 v68, v72, v73 op_sel:[0,0,1]
	v_pk_mul_f32 v[2:3], v[2:3], v[6:7]
	v_med3_f32 v6, v8, s81, v170
	v_med3_f32 v7, v9, s81, v170
	v_pk_add_f32 v[188:189], v[188:189], 1.0 op_sel_hi:[1,0]
	v_cvt_pk_fp8_f32 v54, v52, v53 op_sel:[0,0,1]
	v_pk_mul_f32 v[184:185], v[14:15], v[188:189]
	v_rcp_f32_e32 v184, v184
	v_rcp_f32_e32 v185, v185
	s_nop 0
	v_pk_mul_f32 v[186:187], v[184:185], v[188:189]
	v_pk_mul_f32 v[188:189], v[184:185], v[14:15]
	v_pk_mul_f32 v[2:3], v[2:3], v[186:187]
	v_cvt_pk_fp8_f32 v30, v26, v27
	v_cvt_pk_fp8_f32 v14, v10, v11
	v_cvt_pk_fp8_f32 v15, v2, v3
	ds_write_b64 v108, v[68:69]
	ds_write_b64 v108, v[54:55] offset:768
	v_add_u32_e32 v38, 0x80, v106
	ds_read_b128 v[34:37], v109
	v_pk_mul_f32 v[2:3], v[4:5], v[188:189]
	v_lshl_add_u32 v38, v38, 10, v142
	v_cvt_pk_fp8_f32 v30, v28, v29 op_sel:[0,0,1]
	v_pk_mul_f32 v[2:3], v[2:3], v[6:7]
	v_cvt_pk_fp8_f32 v14, v12, v13 op_sel:[0,0,1]
	v_cvt_pk_fp8_f32 v15, v2, v3 op_sel:[0,0,1]
	s_add_u32 s86, s18, s10
	s_addc_u32 s87, s19, s11
	v_mov_b32_e32 v2, v38
	s_waitcnt lgkmcnt(0)
	global_store_dwordx4 v2, v[34:37], s[86:87]
	ds_write_b64 v108, v[30:31]
	ds_write_b64 v108, v[14:15] offset:768
	v_add_u32_e32 v6, 0xa0, v106
	ds_read_b128 v[2:5], v109
	v_lshl_add_u32 v6, v6, 10, v142
	s_add_u32 s86, s18, s10
	s_addc_u32 s87, s19, s11
	s_and_b64 vcc, exec, s[8:9]
	s_mov_b64 s[8:9], -1
	s_waitcnt lgkmcnt(0)
	global_store_dwordx4 v6, v[2:5], s[86:87]
	s_cbranch_vccnz .LBB0_3339
	s_lshl_b64 s[8:9], s[70:71], 12
	s_add_u32 s11, s6, s8
	s_addc_u32 s65, s7, s9
	s_lshl_b32 s8, s64, 7
	s_ashr_i32 s9, s8, 31
	v_mov_b32_e32 v2, v0
	s_lshl_b64 s[8:9], s[8:9], 1
	s_add_u32 s8, s11, s8
	v_readfirstlane_b32 s10, v2
	s_addc_u32 s9, s65, s9
	s_and_b32 s11, s10, 0xc0
	s_add_u32 s8, s8, s11
	s_addc_u32 s9, s9, 0
	v_and_b32_e32 v3, 48, v2
	global_load_dwordx4 v[46:49], v3, s[8:9]
	global_load_dwordx4 v[42:45], v3, s[8:9] offset:2048
	s_ashr_i32 s9, s10, 2
	s_lshl_b32 s8, s66, 8
	s_andn2_b32 s9, s9, 63
	s_add_i32 s9, s9, s8
	v_and_or_b32 v2, v2, 15, s9
	v_lshlrev_b32_e32 v4, 2, v2
	global_load_dword v179, v4, s[14:15] offset:0
	global_load_dword v178, v4, s[14:15] offset:64
	global_load_dword v177, v4, s[14:15] offset:128
	global_load_dword v176, v4, s[14:15] offset:192
	global_load_dword v175, v4, s[14:15] offset:512
	global_load_dword v174, v4, s[14:15] offset:576
	global_load_dword v171, v4, s[14:15] offset:640
	global_load_dword v169, v4, s[14:15] offset:704
	s_andn2_b64 vcc, exec, s[16:17]
	s_cbranch_vccnz .LBB0_3338
	s_barrier
	s_branch .LBB0_3338

.LBB0_3429:
	v_lshlrev_b32_e32 v158, 16, v6
	v_and_b32_e32 v159, 0xffff0000, v6
	v_lshlrev_b32_e32 v154, 16, v8
	v_and_b32_e32 v155, 0xffff0000, v8
	v_lshlrev_b32_e32 v156, 16, v7
	v_and_b32_e32 v157, 0xffff0000, v7
	v_lshlrev_b32_e32 v152, 16, v9
	v_and_b32_e32 v153, 0xffff0000, v9
	s_waitcnt vmcnt(10)
	v_lshlrev_b32_e32 v6, 16, v4
	v_and_b32_e32 v7, 0xffff0000, v4
	v_mul_f32_e32 v4, 0x41000000, v146
	v_pk_fma_f32 v[134:135], v[134:135], s[38:39], v[158:159] op_sel_hi:[1,0,1]
	v_pk_fma_f32 v[130:131], v[130:131], s[38:39], v[154:155] op_sel_hi:[1,0,1]
	v_pk_fma_f32 v[136:137], v[136:137], s[38:39], v[156:157] op_sel_hi:[1,0,1]
	v_pk_mul_f32 v[134:135], v[4:5], v[134:135] op_sel_hi:[0,1]
	v_pk_fma_f32 v[132:133], v[132:133], s[38:39], v[152:153] op_sel_hi:[1,0,1]
	v_pk_mul_f32 v[130:131], v[4:5], v[130:131] op_sel_hi:[0,1]
	v_lshlrev_b32_e32 v150, 16, v2
	v_and_b32_e32 v151, 0xffff0000, v2
	v_lshlrev_b32_e32 v8, 16, v3
	v_and_b32_e32 v9, 0xffff0000, v3
	v_lshlrev_b32_e32 v2, 16, v5
	v_and_b32_e32 v3, 0xffff0000, v5
	v_pk_mul_f32 v[136:137], v[4:5], v[136:137] op_sel_hi:[0,1]
	v_pk_mul_f32 v[132:133], v[4:5], v[132:133] op_sel_hi:[0,1]
	v_med3_f32 v5, v134, s75, v164
	v_med3_f32 v134, v130, s75, v164
	v_med3_f32 v135, v135, s75, v164
	v_cvt_pk_fp8_f32 v130, v5, v135
	v_med3_f32 v136, v136, s75, v164
	v_med3_f32 v5, v137, s75, v164
	v_pk_fma_f32 v[126:127], v[126:127], s[38:39], v[150:151] op_sel_hi:[1,0,1]
	v_pk_fma_f32 v[128:129], v[128:129], s[38:39], v[8:9] op_sel_hi:[1,0,1]
	v_pk_fma_f32 v[122:123], v[122:123], s[38:39], v[6:7] op_sel_hi:[1,0,1]
	v_pk_fma_f32 v[124:125], v[124:125], s[38:39], v[2:3] op_sel_hi:[1,0,1]
	v_cvt_pk_fp8_f32 v130, v136, v5 op_sel:[0,0,1]
	v_pk_mul_f32 v[128:129], v[4:5], v[128:129] op_sel_hi:[0,1]
	v_pk_mul_f32 v[126:127], v[4:5], v[126:127] op_sel_hi:[0,1]
	v_pk_mul_f32 v[124:125], v[4:5], v[124:125] op_sel_hi:[0,1]
	v_pk_mul_f32 v[4:5], v[4:5], v[122:123] op_sel_hi:[0,1]
	v_med3_f32 v146, v131, s75, v164
	v_med3_f32 v122, v126, s75, v164
	v_med3_f32 v123, v4, s75, v164
	v_med3_f32 v126, v127, s75, v164
	v_med3_f32 v127, v5, s75, v164
	v_cvt_pk_fp8_f32 v131, v134, v146
	v_cvt_pk_fp8_f32 v4, v122, v126
	v_cvt_pk_fp8_f32 v5, v123, v127
	v_mov_b32_e32 v171, v0
	v_med3_f32 v132, v132, s75, v164
	v_readfirstlane_b32 s41, v171
	s_lshr_b32 s8, s41, 6
	v_med3_f32 v133, v133, s75, v164
	v_med3_f32 v128, v128, s75, v164
	v_med3_f32 v124, v124, s75, v164
	v_med3_f32 v122, v129, s75, v164
	v_med3_f32 v123, v125, s75, v164
	s_mulk_i32 s8, 0xb00
	v_cvt_pk_fp8_f32 v131, v132, v133 op_sel:[0,0,1]
	v_cvt_pk_fp8_f32 v4, v128, v122 op_sel:[0,0,1]
	v_cvt_pk_fp8_f32 v5, v124, v123 op_sel:[0,0,1]
	s_add_i32 s8, s8, 0
	v_and_b32_e32 v172, 15, v171
	v_lshrrev_b32_e32 v123, 1, v171
	s_add_i32 s43, s8, 0x20000
	v_mul_u32_u24_e32 v122, 0x50, v172
	v_and_b32_e32 v123, 24, v123
	v_add3_u32 v122, s43, v122, v123
	s_and_b32 s9, s41, 0xc0
	ds_write2_b64 v122, v[130:131], v[4:5] offset1:4
	v_bfe_u32 v4, v171, 2, 4
	s_ashr_i32 s41, s41, 2
	v_mul_u32_u24_e32 v5, 0x50, v4
	v_lshlrev_b32_e32 v123, 4, v171
	s_andn2_b32 s41, s41, 63
	v_lshl_or_b32 v4, s50, 8, v4
	v_and_b32_e32 v146, 48, v123
	v_add_u32_e32 v4, s41, v4
	v_mul_f32_e32 v130, 0x41000000, v170
	v_pk_fma_f32 v[118:119], v[118:119], s[38:39], v[158:159] op_sel_hi:[1,0,1]
	v_pk_fma_f32 v[114:115], v[114:115], s[38:39], v[154:155] op_sel_hi:[1,0,1]
	v_add3_u32 v123, s43, v5, v146
	v_pk_mul_f32 v[118:119], v[130:131], v[118:119] op_sel_hi:[0,1]
	v_pk_mul_f32 v[114:115], v[130:131], v[114:115] op_sel_hi:[0,1]
	v_lshl_add_u32 v128, v4, 10, v146
	v_med3_f32 v5, v118, s75, v164
	v_med3_f32 v118, v114, s75, v164
	v_med3_f32 v119, v119, s75, v164
	v_cvt_pk_fp8_f32 v114, v5, v119
	v_pk_fma_f32 v[120:121], v[120:121], s[38:39], v[156:157] op_sel_hi:[1,0,1]
	v_pk_fma_f32 v[116:117], v[116:117], s[38:39], v[152:153] op_sel_hi:[1,0,1]
	v_pk_mul_f32 v[120:121], v[130:131], v[120:121] op_sel_hi:[0,1]
	v_pk_mul_f32 v[116:117], v[130:131], v[116:117] op_sel_hi:[0,1]
	v_med3_f32 v131, v115, s75, v164
	v_pk_fma_f32 v[110:111], v[110:111], s[38:39], v[150:151] op_sel_hi:[1,0,1]
	v_pk_fma_f32 v[106:107], v[106:107], s[38:39], v[6:7] op_sel_hi:[1,0,1]
	v_med3_f32 v120, v120, s75, v164
	v_med3_f32 v5, v121, s75, v164
	v_pk_mul_f32 v[110:111], v[130:131], v[110:111] op_sel_hi:[0,1]
	v_pk_mul_f32 v[106:107], v[130:131], v[106:107] op_sel_hi:[0,1]
	v_cvt_pk_fp8_f32 v114, v120, v5 op_sel:[0,0,1]
	v_med3_f32 v5, v110, s75, v164
	v_med3_f32 v110, v106, s75, v164
	v_med3_f32 v111, v111, s75, v164
	v_cvt_pk_fp8_f32 v106, v5, v111
	v_pk_fma_f32 v[112:113], v[112:113], s[38:39], v[8:9] op_sel_hi:[1,0,1]
	v_pk_mul_f32 v[112:113], v[130:131], v[112:113] op_sel_hi:[0,1]
	v_med3_f32 v112, v112, s75, v164
	v_med3_f32 v5, v113, s75, v164
	v_cvt_pk_fp8_f32 v106, v112, v5 op_sel:[0,0,1]
	v_mul_f32_e32 v112, 0x41000000, v169
	v_pk_fma_f32 v[102:103], v[102:103], s[38:39], v[158:159] op_sel_hi:[1,0,1]
	v_pk_fma_f32 v[98:99], v[98:99], s[38:39], v[154:155] op_sel_hi:[1,0,1]
	v_cvt_pk_fp8_f32 v115, v118, v131
	v_pk_mul_f32 v[102:103], v[112:113], v[102:103] op_sel_hi:[0,1]
	v_pk_mul_f32 v[98:99], v[112:113], v[98:99] op_sel_hi:[0,1]
	v_med3_f32 v5, v102, s75, v164
	v_med3_f32 v102, v98, s75, v164
	v_med3_f32 v103, v103, s75, v164
	v_cvt_pk_fp8_f32 v98, v5, v103
	v_med3_f32 v116, v116, s75, v164
	v_med3_f32 v117, v117, s75, v164
	v_pk_fma_f32 v[104:105], v[104:105], s[38:39], v[156:157] op_sel_hi:[1,0,1]
	v_pk_fma_f32 v[100:101], v[100:101], s[38:39], v[152:153] op_sel_hi:[1,0,1]
	v_cvt_pk_fp8_f32 v115, v116, v117 op_sel:[0,0,1]
	v_med3_f32 v116, v107, s75, v164
	v_pk_mul_f32 v[104:105], v[112:113], v[104:105] op_sel_hi:[0,1]
	v_pk_mul_f32 v[100:101], v[112:113], v[100:101] op_sel_hi:[0,1]
	v_med3_f32 v113, v99, s75, v164
	v_pk_fma_f32 v[94:95], v[94:95], s[38:39], v[150:151] op_sel_hi:[1,0,1]
	v_pk_fma_f32 v[90:91], v[90:91], s[38:39], v[6:7] op_sel_hi:[1,0,1]
	v_cvt_pk_fp8_f32 v107, v110, v116
	v_med3_f32 v104, v104, s75, v164
	v_med3_f32 v5, v105, s75, v164
	v_pk_mul_f32 v[94:95], v[112:113], v[94:95] op_sel_hi:[0,1]
	v_pk_mul_f32 v[90:91], v[112:113], v[90:91] op_sel_hi:[0,1]
	v_pk_fma_f32 v[108:109], v[108:109], s[38:39], v[2:3] op_sel_hi:[1,0,1]
	v_cvt_pk_fp8_f32 v98, v104, v5 op_sel:[0,0,1]
	v_med3_f32 v5, v94, s75, v164
	v_med3_f32 v94, v90, s75, v164
	v_med3_f32 v95, v95, s75, v164
	s_lshl_b32 s8, s62, 8
	ds_read_b128 v[124:127], v123
	v_pk_mul_f32 v[108:109], v[130:131], v[108:109] op_sel_hi:[0,1]
	v_cvt_pk_fp8_f32 v99, v102, v113
	v_cvt_pk_fp8_f32 v90, v5, v95
	s_or_b32 s8, s9, s8
	v_med3_f32 v108, v108, s75, v164
	v_med3_f32 v109, v109, s75, v164
	v_pk_fma_f32 v[96:97], v[96:97], s[38:39], v[8:9] op_sel_hi:[1,0,1]
	s_ashr_i32 s9, s8, 31
	v_cvt_pk_fp8_f32 v107, v108, v109 op_sel:[0,0,1]
	v_pk_mul_f32 v[96:97], v[112:113], v[96:97] op_sel_hi:[0,1]
	s_add_u32 s86, s16, s8
	s_addc_u32 s87, s17, s9
	v_med3_f32 v100, v100, s75, v164
	v_med3_f32 v101, v101, s75, v164
	v_med3_f32 v96, v96, s75, v164
	v_med3_f32 v5, v97, s75, v164
	v_mov_b32_e32 v108, v128
	v_cvt_pk_fp8_f32 v99, v100, v101 op_sel:[0,0,1]
	v_med3_f32 v100, v91, s75, v164
	v_cvt_pk_fp8_f32 v90, v96, v5 op_sel:[0,0,1]
	v_mul_f32_e32 v96, 0x41000000, v168
	v_pk_fma_f32 v[78:79], v[78:79], s[38:39], v[158:159] op_sel_hi:[1,0,1]
	v_pk_fma_f32 v[74:75], v[74:75], s[38:39], v[154:155] op_sel_hi:[1,0,1]
	s_waitcnt lgkmcnt(0)
	global_store_dwordx4 v108, v[124:127], s[86:87]
	v_cvt_pk_fp8_f32 v91, v94, v100
	v_pk_fma_f32 v[80:81], v[80:81], s[38:39], v[156:157] op_sel_hi:[1,0,1]
	v_pk_mul_f32 v[78:79], v[96:97], v[78:79] op_sel_hi:[0,1]
	v_pk_fma_f32 v[76:77], v[76:77], s[38:39], v[152:153] op_sel_hi:[1,0,1]
	v_pk_mul_f32 v[74:75], v[96:97], v[74:75] op_sel_hi:[0,1]
	ds_write2_b64 v122, v[114:115], v[106:107] offset1:4
	v_or_b32_e32 v110, 16, v4
	v_pk_fma_f32 v[92:93], v[92:93], s[38:39], v[2:3] op_sel_hi:[1,0,1]
	v_pk_mul_f32 v[80:81], v[96:97], v[80:81] op_sel_hi:[0,1]
	v_pk_mul_f32 v[76:77], v[96:97], v[76:77] op_sel_hi:[0,1]
	v_med3_f32 v5, v78, s75, v164
	v_med3_f32 v78, v74, s75, v164
	v_med3_f32 v79, v79, s75, v164
	v_med3_f32 v97, v75, s75, v164
	ds_read_b128 v[106:109], v123
	v_pk_mul_f32 v[92:93], v[112:113], v[92:93] op_sel_hi:[0,1]
	v_cvt_pk_fp8_f32 v74, v5, v79
	v_cvt_pk_fp8_f32 v75, v78, v97
	v_lshl_add_u32 v110, v110, 10, v146
	v_med3_f32 v92, v92, s75, v164
	v_med3_f32 v93, v93, s75, v164
	v_cvt_pk_fp8_f32 v91, v92, v93 op_sel:[0,0,1]
	v_pk_fma_f32 v[62:63], v[62:63], s[38:39], v[150:151] op_sel_hi:[1,0,1]
	v_pk_fma_f32 v[58:59], v[58:59], s[38:39], v[6:7] op_sel_hi:[1,0,1]
	s_add_u32 s86, s16, s8
	s_addc_u32 s87, s17, s9
	v_med3_f32 v80, v80, s75, v164
	v_med3_f32 v76, v76, s75, v164
	v_med3_f32 v5, v81, s75, v164
	v_med3_f32 v77, v77, s75, v164
	v_pk_mul_f32 v[62:63], v[96:97], v[62:63] op_sel_hi:[0,1]
	v_pk_mul_f32 v[58:59], v[96:97], v[58:59] op_sel_hi:[0,1]
	v_mov_b32_e32 v92, v110
	v_cvt_pk_fp8_f32 v74, v80, v5 op_sel:[0,0,1]
	v_cvt_pk_fp8_f32 v75, v76, v77 op_sel:[0,0,1]
	v_med3_f32 v5, v62, s75, v164
	v_med3_f32 v62, v58, s75, v164
	v_med3_f32 v63, v63, s75, v164
	v_med3_f32 v76, v59, s75, v164
	s_waitcnt lgkmcnt(0)
	global_store_dwordx4 v92, v[106:109], s[86:87]
	v_cvt_pk_fp8_f32 v58, v5, v63
	v_cvt_pk_fp8_f32 v59, v62, v76
	ds_write2_b64 v122, v[98:99], v[90:91] offset1:4
	v_or_b32_e32 v94, 32, v4
	v_pk_fma_f32 v[64:65], v[64:65], s[38:39], v[8:9] op_sel_hi:[1,0,1]
	v_pk_fma_f32 v[60:61], v[60:61], s[38:39], v[2:3] op_sel_hi:[1,0,1]
	ds_read_b128 v[90:93], v123
	v_pk_mul_f32 v[64:65], v[96:97], v[64:65] op_sel_hi:[0,1]
	v_pk_mul_f32 v[60:61], v[96:97], v[60:61] op_sel_hi:[0,1]
	v_lshl_add_u32 v94, v94, 10, v146
	v_med3_f32 v64, v64, s75, v164
	v_med3_f32 v60, v60, s75, v164
	v_med3_f32 v5, v65, s75, v164
	v_med3_f32 v61, v61, s75, v164
	v_cvt_pk_fp8_f32 v58, v64, v5 op_sel:[0,0,1]
	v_cvt_pk_fp8_f32 v59, v60, v61 op_sel:[0,0,1]
	s_add_u32 s86, s16, s8
	s_addc_u32 s87, s17, s9
	v_mov_b32_e32 v60, v94
	s_waitcnt lgkmcnt(0)
	global_store_dwordx4 v60, v[90:93], s[86:87]
	ds_write2_b64 v122, v[74:75], v[58:59] offset1:4
	v_mul_f32_e32 v64, 0x41000000, v167
	v_pk_fma_f32 v[74:75], v[86:87], s[38:39], v[158:159] op_sel_hi:[1,0,1]
	v_pk_fma_f32 v[78:79], v[82:83], s[38:39], v[154:155] op_sel_hi:[1,0,1]
	v_pk_mul_f32 v[74:75], v[64:65], v[74:75] op_sel_hi:[0,1]
	v_pk_fma_f32 v[76:77], v[88:89], s[38:39], v[156:157] op_sel_hi:[1,0,1]
	v_pk_fma_f32 v[80:81], v[84:85], s[38:39], v[152:153] op_sel_hi:[1,0,1]
	v_pk_mul_f32 v[78:79], v[64:65], v[78:79] op_sel_hi:[0,1]
	v_med3_f32 v5, v74, s75, v164
	v_med3_f32 v75, v75, s75, v164
	v_pk_mul_f32 v[76:77], v[64:65], v[76:77] op_sel_hi:[0,1]
	v_pk_mul_f32 v[80:81], v[64:65], v[80:81] op_sel_hi:[0,1]
	v_med3_f32 v65, v78, s75, v164
	v_med3_f32 v78, v79, s75, v164
	v_cvt_pk_fp8_f32 v74, v5, v75
	v_cvt_pk_fp8_f32 v75, v65, v78
	v_med3_f32 v79, v80, s75, v164
	v_med3_f32 v65, v81, s75, v164
	v_pk_fma_f32 v[70:71], v[70:71], s[38:39], v[150:151] op_sel_hi:[1,0,1]
	v_pk_fma_f32 v[72:73], v[72:73], s[38:39], v[8:9] op_sel_hi:[1,0,1]
	v_pk_fma_f32 v[66:67], v[66:67], s[38:39], v[6:7] op_sel_hi:[1,0,1]
	v_pk_fma_f32 v[68:69], v[68:69], s[38:39], v[2:3] op_sel_hi:[1,0,1]
	v_med3_f32 v76, v76, s75, v164
	v_med3_f32 v5, v77, s75, v164
	v_cvt_pk_fp8_f32 v75, v79, v65 op_sel:[0,0,1]
	v_pk_mul_f32 v[72:73], v[64:65], v[72:73] op_sel_hi:[0,1]
	v_pk_mul_f32 v[70:71], v[64:65], v[70:71] op_sel_hi:[0,1]
	v_pk_mul_f32 v[68:69], v[64:65], v[68:69] op_sel_hi:[0,1]
	v_pk_mul_f32 v[64:65], v[64:65], v[66:67] op_sel_hi:[0,1]
	v_cvt_pk_fp8_f32 v74, v76, v5 op_sel:[0,0,1]
	v_med3_f32 v5, v70, s75, v164
	v_med3_f32 v66, v64, s75, v164
	v_med3_f32 v67, v71, s75, v164
	v_med3_f32 v70, v65, s75, v164
	v_cvt_pk_fp8_f32 v64, v5, v67
	v_cvt_pk_fp8_f32 v65, v66, v70
	v_or_b32_e32 v62, 48, v4
	ds_read_b128 v[58:61], v123
	v_lshl_add_u32 v62, v62, 10, v146
	v_med3_f32 v71, v72, s75, v164
	v_med3_f32 v68, v68, s75, v164
	v_med3_f32 v5, v73, s75, v164
	v_med3_f32 v66, v69, s75, v164
	v_cvt_pk_fp8_f32 v64, v71, v5 op_sel:[0,0,1]
	v_cvt_pk_fp8_f32 v65, v68, v66 op_sel:[0,0,1]
	s_add_u32 s86, s16, s8
	s_addc_u32 s87, s17, s9
	s_waitcnt lgkmcnt(0)
	global_store_dwordx4 v62, v[58:61], s[86:87]
	ds_write2_b64 v122, v[74:75], v[64:65] offset1:4
	v_mul_f32_e32 v64, 0x41000000, v166
	v_pk_fma_f32 v[54:55], v[54:55], s[38:39], v[158:159] op_sel_hi:[1,0,1]
	v_pk_fma_f32 v[50:51], v[50:51], s[38:39], v[154:155] op_sel_hi:[1,0,1]
	v_pk_mul_f32 v[54:55], v[64:65], v[54:55] op_sel_hi:[0,1]
	v_pk_mul_f32 v[50:51], v[64:65], v[50:51] op_sel_hi:[0,1]
	v_med3_f32 v5, v54, s75, v164
	v_med3_f32 v54, v50, s75, v164
	v_med3_f32 v55, v55, s75, v164
	v_cvt_pk_fp8_f32 v50, v5, v55
	v_pk_fma_f32 v[56:57], v[56:57], s[38:39], v[156:157] op_sel_hi:[1,0,1]
	v_pk_fma_f32 v[52:53], v[52:53], s[38:39], v[152:153] op_sel_hi:[1,0,1]
	v_pk_mul_f32 v[56:57], v[64:65], v[56:57] op_sel_hi:[0,1]
	v_pk_mul_f32 v[52:53], v[64:65], v[52:53] op_sel_hi:[0,1]
	v_med3_f32 v65, v51, s75, v164
	v_pk_fma_f32 v[46:47], v[46:47], s[38:39], v[150:151] op_sel_hi:[1,0,1]
	v_pk_fma_f32 v[42:43], v[42:43], s[38:39], v[6:7] op_sel_hi:[1,0,1]
	v_med3_f32 v56, v56, s75, v164
	v_med3_f32 v5, v57, s75, v164
	v_pk_mul_f32 v[46:47], v[64:65], v[46:47] op_sel_hi:[0,1]
	v_pk_mul_f32 v[42:43], v[64:65], v[42:43] op_sel_hi:[0,1]
	v_cvt_pk_fp8_f32 v50, v56, v5 op_sel:[0,0,1]
	v_med3_f32 v5, v46, s75, v164
	v_med3_f32 v46, v42, s75, v164
	v_med3_f32 v47, v47, s75, v164
	v_cvt_pk_fp8_f32 v42, v5, v47
	v_pk_fma_f32 v[48:49], v[48:49], s[38:39], v[8:9] op_sel_hi:[1,0,1]
	v_pk_mul_f32 v[48:49], v[64:65], v[48:49] op_sel_hi:[0,1]
	v_med3_f32 v48, v48, s75, v164
	v_med3_f32 v5, v49, s75, v164
	v_cvt_pk_fp8_f32 v42, v48, v5 op_sel:[0,0,1]
	v_mul_f32_e32 v48, 0x41000000, v165
	v_pk_fma_f32 v[38:39], v[38:39], s[38:39], v[158:159] op_sel_hi:[1,0,1]
	v_pk_fma_f32 v[34:35], v[34:35], s[38:39], v[154:155] op_sel_hi:[1,0,1]
	v_cvt_pk_fp8_f32 v51, v54, v65
	v_pk_mul_f32 v[38:39], v[48:49], v[38:39] op_sel_hi:[0,1]
	v_pk_mul_f32 v[34:35], v[48:49], v[34:35] op_sel_hi:[0,1]
	v_med3_f32 v5, v38, s75, v164
	v_med3_f32 v38, v34, s75, v164
	v_med3_f32 v39, v39, s75, v164
	v_cvt_pk_fp8_f32 v34, v5, v39
	v_med3_f32 v52, v52, s75, v164
	v_med3_f32 v53, v53, s75, v164
	v_pk_fma_f32 v[40:41], v[40:41], s[38:39], v[156:157] op_sel_hi:[1,0,1]
	v_pk_fma_f32 v[36:37], v[36:37], s[38:39], v[152:153] op_sel_hi:[1,0,1]
	v_cvt_pk_fp8_f32 v51, v52, v53 op_sel:[0,0,1]
	v_med3_f32 v52, v43, s75, v164
	v_pk_mul_f32 v[40:41], v[48:49], v[40:41] op_sel_hi:[0,1]
	v_pk_mul_f32 v[36:37], v[48:49], v[36:37] op_sel_hi:[0,1]
	v_med3_f32 v49, v35, s75, v164
	v_pk_fma_f32 v[30:31], v[30:31], s[38:39], v[150:151] op_sel_hi:[1,0,1]
	v_pk_fma_f32 v[26:27], v[26:27], s[38:39], v[6:7] op_sel_hi:[1,0,1]
	v_cvt_pk_fp8_f32 v43, v46, v52
	v_med3_f32 v40, v40, s75, v164
	v_med3_f32 v5, v41, s75, v164
	v_pk_mul_f32 v[30:31], v[48:49], v[30:31] op_sel_hi:[0,1]
	v_pk_mul_f32 v[26:27], v[48:49], v[26:27] op_sel_hi:[0,1]
	v_add_u32_e32 v62, 0x80, v4
	v_pk_fma_f32 v[44:45], v[44:45], s[38:39], v[2:3] op_sel_hi:[1,0,1]
	v_cvt_pk_fp8_f32 v34, v40, v5 op_sel:[0,0,1]
	v_med3_f32 v5, v30, s75, v164
	v_med3_f32 v30, v26, s75, v164
	v_med3_f32 v31, v31, s75, v164
	ds_read_b128 v[58:61], v123
	v_pk_mul_f32 v[44:45], v[64:65], v[44:45] op_sel_hi:[0,1]
	v_cvt_pk_fp8_f32 v35, v38, v49
	v_cvt_pk_fp8_f32 v26, v5, v31
	v_lshl_add_u32 v62, v62, 10, v146
	v_med3_f32 v44, v44, s75, v164
	v_med3_f32 v45, v45, s75, v164
	v_pk_fma_f32 v[32:33], v[32:33], s[38:39], v[8:9] op_sel_hi:[1,0,1]
	v_cvt_pk_fp8_f32 v43, v44, v45 op_sel:[0,0,1]
	v_pk_mul_f32 v[32:33], v[48:49], v[32:33] op_sel_hi:[0,1]
	s_add_u32 s86, s16, s8
	s_addc_u32 s87, s17, s9
	v_med3_f32 v36, v36, s75, v164
	v_med3_f32 v37, v37, s75, v164
	v_med3_f32 v32, v32, s75, v164
	v_med3_f32 v5, v33, s75, v164
	v_mov_b32_e32 v44, v62
	v_cvt_pk_fp8_f32 v35, v36, v37 op_sel:[0,0,1]
	v_med3_f32 v36, v27, s75, v164
	v_cvt_pk_fp8_f32 v26, v32, v5 op_sel:[0,0,1]
	v_mul_f32_e32 v32, 0x41000000, v1
	v_pk_fma_f32 v[22:23], v[22:23], s[38:39], v[158:159] op_sel_hi:[1,0,1]
	v_pk_fma_f32 v[18:19], v[18:19], s[38:39], v[154:155] op_sel_hi:[1,0,1]
	s_waitcnt lgkmcnt(0)
	global_store_dwordx4 v44, v[58:61], s[86:87]
	v_cvt_pk_fp8_f32 v27, v30, v36
	v_pk_mul_f32 v[22:23], v[32:33], v[22:23] op_sel_hi:[0,1]
	v_pk_mul_f32 v[18:19], v[32:33], v[18:19] op_sel_hi:[0,1]
	ds_write2_b64 v122, v[50:51], v[42:43] offset1:4
	v_add_u32_e32 v46, 0x90, v4
	v_pk_fma_f32 v[28:29], v[28:29], s[38:39], v[2:3] op_sel_hi:[1,0,1]
	v_med3_f32 v1, v22, s75, v164
	v_med3_f32 v5, v18, s75, v164
	v_med3_f32 v22, v23, s75, v164
	v_med3_f32 v23, v19, s75, v164
	ds_read_b128 v[42:45], v123
	v_pk_mul_f32 v[28:29], v[48:49], v[28:29] op_sel_hi:[0,1]
	v_cvt_pk_fp8_f32 v18, v1, v22
	v_cvt_pk_fp8_f32 v19, v5, v23
	v_lshl_add_u32 v46, v46, 10, v146
	v_med3_f32 v28, v28, s75, v164
	v_med3_f32 v29, v29, s75, v164
	v_pk_fma_f32 v[24:25], v[24:25], s[38:39], v[156:157] op_sel_hi:[1,0,1]
	v_pk_fma_f32 v[20:21], v[20:21], s[38:39], v[152:153] op_sel_hi:[1,0,1]
	v_cvt_pk_fp8_f32 v27, v28, v29 op_sel:[0,0,1]
	v_pk_mul_f32 v[24:25], v[32:33], v[24:25] op_sel_hi:[0,1]
	v_pk_mul_f32 v[20:21], v[32:33], v[20:21] op_sel_hi:[0,1]
	v_pk_fma_f32 v[14:15], v[14:15], s[38:39], v[150:151] op_sel_hi:[1,0,1]
	v_pk_fma_f32 v[6:7], v[10:11], s[38:39], v[6:7] op_sel_hi:[1,0,1]
	s_add_u32 s86, s16, s8
	s_addc_u32 s87, s17, s9
	v_med3_f32 v24, v24, s75, v164
	v_med3_f32 v20, v20, s75, v164
	v_med3_f32 v1, v25, s75, v164
	v_med3_f32 v5, v21, s75, v164
	v_pk_mul_f32 v[14:15], v[32:33], v[14:15] op_sel_hi:[0,1]
	v_pk_mul_f32 v[6:7], v[32:33], v[6:7] op_sel_hi:[0,1]
	v_mov_b32_e32 v28, v46
	v_cvt_pk_fp8_f32 v18, v24, v1 op_sel:[0,0,1]
	v_cvt_pk_fp8_f32 v19, v20, v5 op_sel:[0,0,1]
	v_med3_f32 v1, v14, s75, v164
	v_med3_f32 v5, v6, s75, v164
	v_med3_f32 v10, v15, s75, v164
	v_med3_f32 v11, v7, s75, v164
	s_waitcnt lgkmcnt(0)
	global_store_dwordx4 v28, v[42:45], s[86:87]
	v_cvt_pk_fp8_f32 v6, v1, v10
	v_cvt_pk_fp8_f32 v7, v5, v11
	ds_write2_b64 v122, v[34:35], v[26:27] offset1:4
	v_add_u32_e32 v30, 0xa0, v4
	v_pk_fma_f32 v[8:9], v[16:17], s[38:39], v[8:9] op_sel_hi:[1,0,1]
	v_pk_fma_f32 v[2:3], v[12:13], s[38:39], v[2:3] op_sel_hi:[1,0,1]
	ds_read_b128 v[26:29], v123
	v_pk_mul_f32 v[8:9], v[32:33], v[8:9] op_sel_hi:[0,1]
	v_pk_mul_f32 v[2:3], v[32:33], v[2:3] op_sel_hi:[0,1]
	v_lshl_add_u32 v30, v30, 10, v146
	v_med3_f32 v8, v8, s75, v164
	v_med3_f32 v2, v2, s75, v164
	v_med3_f32 v1, v9, s75, v164
	v_med3_f32 v3, v3, s75, v164
	v_cvt_pk_fp8_f32 v6, v8, v1 op_sel:[0,0,1]
	v_cvt_pk_fp8_f32 v7, v2, v3 op_sel:[0,0,1]
	s_add_u32 s86, s16, s8
	s_addc_u32 s87, s17, s9
	v_mov_b32_e32 v2, v30
	s_waitcnt lgkmcnt(0)
	global_store_dwordx4 v2, v[26:29], s[86:87]
	ds_write2_b64 v122, v[18:19], v[6:7] offset1:4
	v_add_u32_e32 v2, 0xb0, v4
	ds_read_b128 v[6:9], v123
	v_ashrrev_i32_e32 v3, 31, v2
	v_lshl_add_u32 v2, v2, 10, v146
	s_add_u32 s86, s16, s8
	s_addc_u32 s87, s17, s9
	s_waitcnt lgkmcnt(0)
	global_store_dwordx4 v2, v[6:9], s[86:87]
	s_and_b64 vcc, exec, s[10:11]
	s_mov_b64 s[8:9], -1
	s_cbranch_vccnz .LBB0_3418
	v_mov_b32_e32 v12, v0
	s_lshl_b32 s9, s42, 8
	v_readfirstlane_b32 s8, v12
	s_and_b32 s10, s8, 0xc0
	s_ashr_i32 s8, s8, 2
	s_andn2_b32 s8, s8, 63
	s_add_i32 s8, s8, s9
	v_and_or_b32 v2, v12, 15, s8
	v_lshlrev_b32_e32 v4, 2, v2
	s_lshl_b64 s[8:9], s[44:45], 11
	s_add_u32 s11, s54, s8
	s_addc_u32 s41, s55, s9
	s_lshl_b32 s8, s40, 8
	global_load_dword v146, v4, s[12:13] offset:0
	global_load_dword v170, v4, s[12:13] offset:64
	global_load_dword v169, v4, s[12:13] offset:128
	global_load_dword v168, v4, s[12:13] offset:192
	global_load_dword v167, v4, s[12:13] offset:512
	global_load_dword v166, v4, s[12:13] offset:576
	global_load_dword v165, v4, s[12:13] offset:640
	global_load_dword v1, v4, s[12:13] offset:704
	s_ashr_i32 s9, s8, 31
	s_lshl_b64 s[8:9], s[8:9], 1
	s_add_u32 s8, s11, s8
	s_addc_u32 s9, s41, s9
	s_lshl_b32 s10, s10, 1
	s_add_u32 s8, s8, s10
	s_addc_u32 s9, s9, 0
	v_and_b32_e32 v2, 48, v12
	global_load_dwordx4 v[6:9], v2, s[8:9]
	s_nop 0
	global_load_dwordx4 v[2:5], v2, s[8:9] offset:64
	s_andn2_b64 vcc, exec, s[14:15]
	s_cbranch_vccnz .LBB0_3417
	s_barrier
	s_branch .LBB0_3417
